# fp8 pack sequences: dead zero-initialisations ahead of the v_cvt_pk_fp8_f32 low/high pairs dropped (SwiGLU epilogues, quantise loop)
# baseline (speedup 1.0000x reference)
.LBB0_474:
	v_lshl_add_u32 v152, s24, 8, v156
	v_ashrrev_i32_e32 v153, 31, v152
	v_lshl_add_u64 v[154:155], v[152:153], 3, s[10:11]
	global_load_dwordx2 v[166:167], v[154:155], off
	global_load_dwordx2 v[178:179], v[154:155], off offset:128
	global_load_dwordx2 v[180:181], v[154:155], off offset:256
	global_load_dwordx2 v[182:183], v[154:155], off offset:384
	global_load_dwordx2 v[184:185], v[154:155], off offset:1024
	global_load_dwordx2 v[186:187], v[154:155], off offset:1152
	global_load_dwordx2 v[188:189], v[154:155], off offset:1280
	global_load_dwordx2 v[190:191], v[154:155], off offset:1408
	v_pk_mul_f32 v[126:127], v[118:119], v[126:127]
	v_pk_mul_f32 v[122:123], v[114:115], v[122:123]
	v_pk_mul_f32 v[128:129], v[120:121], v[128:129]
	v_pk_mul_f32 v[124:125], v[116:117], v[124:125]
	v_mov_b32_e32 v168, 0
	v_mov_b32_e32 v169, 0
	v_lshl_or_b32 v148, s54, 7, v159
	v_mov_b64_e32 v[150:151], s[8:9]
	v_or_b32_e32 v170, 16, v152
	v_ashrrev_i32_e32 v171, 31, v170
	v_pk_mul_f32 v[110:111], v[102:103], v[110:111]
	v_pk_mul_f32 v[106:107], v[98:99], v[106:107]
	v_pk_mul_f32 v[112:113], v[104:105], v[112:113]
	v_pk_mul_f32 v[108:109], v[100:101], v[108:109]
	v_pk_mul_f32 v[94:95], v[86:87], v[94:95]
	v_pk_mul_f32 v[90:91], v[82:83], v[90:91]
	v_pk_mul_f32 v[96:97], v[88:89], v[96:97]
	v_pk_mul_f32 v[92:93], v[84:85], v[92:93]
	v_pk_mul_f32 v[78:79], v[74:75], v[78:79]
	v_pk_mul_f32 v[66:67], v[70:71], v[66:67]
	v_pk_mul_f32 v[80:81], v[76:77], v[80:81]
	v_pk_mul_f32 v[68:69], v[72:73], v[68:69]
	v_pk_mul_f32 v[62:63], v[58:59], v[62:63]
	v_pk_mul_f32 v[50:51], v[54:55], v[50:51]
	v_pk_mul_f32 v[64:65], v[60:61], v[64:65]
	v_pk_mul_f32 v[52:53], v[56:57], v[52:53]
	v_pk_mul_f32 v[46:47], v[42:43], v[46:47]
	v_pk_mul_f32 v[34:35], v[38:39], v[34:35]
	v_pk_mul_f32 v[48:49], v[44:45], v[48:49]
	v_pk_mul_f32 v[36:37], v[40:41], v[36:37]
	v_pk_mul_f32 v[30:31], v[26:27], v[30:31]
	v_pk_mul_f32 v[18:19], v[22:23], v[18:19]
	v_pk_mul_f32 v[32:33], v[28:29], v[32:33]
	v_pk_mul_f32 v[20:21], v[24:25], v[20:21]
	v_pk_mul_f32 v[14:15], v[6:7], v[14:15]
	v_pk_mul_f32 v[10:11], v[2:3], v[10:11]
	v_pk_mul_f32 v[16:17], v[8:9], v[16:17]
	v_pk_mul_f32 v[12:13], v[4:5], v[12:13]
	s_andn2_b64 vcc, exec, s[4:5]
	s_mov_b64 s[4:5], -1
	s_waitcnt vmcnt(7)
	v_ffbh_u32_e32 v149, v167
	v_min_u32_e32 v153, 32, v149
	v_lshlrev_b64 v[166:167], v153, v[166:167]
	v_min_u32_e32 v149, 1, v166
	v_or_b32_e32 v149, v167, v149
	v_cvt_f32_u32_e32 v165, v149
	v_sub_u32_e32 v153, 32, v153
	v_ashrrev_i32_e32 v149, 31, v148
	v_mad_i64_i32 v[166:167], s[26:27], v152, s48, v[150:151]
	v_ldexp_f32 v153, v165, v153
	v_fmamk_f32 v153, v153, 0x30000000, v163
	v_rsq_f32_e32 v165, v153
	v_mul_f32_e32 v172, 0x3e000000, v153
	v_mul_f32_e32 v174, 0xbfb8aa3b, v165
	v_pk_mul_f32 v[118:119], v[118:119], v[174:175] op_sel_hi:[1,0]
	v_pk_mul_f32 v[114:115], v[114:115], v[174:175] op_sel_hi:[1,0]
	v_exp_f32_e32 v118, v118
	v_exp_f32_e32 v119, v119
	v_exp_f32_e32 v114, v114
	v_exp_f32_e32 v115, v115
	v_pk_mul_f32 v[120:121], v[120:121], v[174:175] op_sel_hi:[1,0]
	v_pk_mul_f32 v[116:117], v[116:117], v[174:175] op_sel_hi:[1,0]
	v_exp_f32_e32 v120, v120
	v_exp_f32_e32 v121, v121
	v_exp_f32_e32 v116, v116
	v_exp_f32_e32 v117, v117
	v_pk_fma_f32 v[118:119], v[172:173], v[118:119], v[172:173] op_sel_hi:[0,1,0]
	v_pk_fma_f32 v[114:115], v[172:173], v[114:115], v[172:173] op_sel_hi:[0,1,0]
	v_rcp_f32_e32 v118, v118
	v_rcp_f32_e32 v119, v119
	v_rcp_f32_e32 v114, v114
	v_rcp_f32_e32 v115, v115
	v_pk_fma_f32 v[120:121], v[172:173], v[120:121], v[172:173] op_sel_hi:[0,1,0]
	v_pk_fma_f32 v[116:117], v[172:173], v[116:117], v[172:173] op_sel_hi:[0,1,0]
	v_rcp_f32_e32 v120, v120
	v_rcp_f32_e32 v121, v121
	v_rcp_f32_e32 v116, v116
	v_rcp_f32_e32 v117, v117
	v_pk_mul_f32 v[118:119], v[126:127], v[118:119]
	v_pk_mul_f32 v[114:115], v[122:123], v[114:115]
	v_med3_f32 v118, v118, s49, v164
	v_med3_f32 v119, v119, s49, v164
	v_med3_f32 v114, v114, s49, v164
	v_med3_f32 v115, v115, s49, v164
	v_cvt_pk_fp8_f32 v168, v118, v119
	v_cvt_pk_fp8_f32 v169, v114, v115
	v_pk_mul_f32 v[120:121], v[128:129], v[120:121]
	v_pk_mul_f32 v[116:117], v[124:125], v[116:117]
	v_med3_f32 v120, v120, s49, v164
	v_med3_f32 v121, v121, s49, v164
	v_med3_f32 v114, v116, s49, v164
	v_med3_f32 v115, v117, s49, v164
	v_cvt_pk_fp8_f32 v168, v120, v121 op_sel:[0,0,1]
	v_cvt_pk_fp8_f32 v169, v114, v115 op_sel:[0,0,1]
	v_lshl_add_u64 v[114:115], v[166:167], 0, v[148:149]
	v_lshl_add_u64 v[116:117], v[170:171], 3, s[10:11]
	global_store_dwordx2 v[114:115], v[168:169], off
	s_nop 0
	s_nop 0
	s_waitcnt vmcnt(7)
	v_mov_b32_e32 v114, v178
	v_mov_b32_e32 v115, v179
	v_ffbh_u32_e32 v117, v115
	v_min_u32_e32 v118, 32, v117
	v_lshlrev_b64 v[114:115], v118, v[114:115]
	v_min_u32_e32 v114, 1, v114
	v_or_b32_e32 v114, v115, v114
	v_cvt_f32_u32_e32 v115, v114
	v_sub_u32_e32 v118, 32, v118
	s_nop 0
	v_or_b32_e32 v114, 32, v152
	v_ldexp_f32 v115, v115, v118
	v_fmamk_f32 v115, v115, 0x30000000, v163
	v_rsq_f32_e32 v121, v115
	v_mul_f32_e32 v120, 0x3e000000, v115
	v_mad_i64_i32 v[118:119], s[26:27], v170, s48, v[150:151]
	v_mul_f32_e32 v122, 0xbfb8aa3b, v121
	v_pk_mul_f32 v[102:103], v[102:103], v[122:123] op_sel_hi:[1,0]
	v_pk_mul_f32 v[98:99], v[98:99], v[122:123] op_sel_hi:[1,0]
	v_exp_f32_e32 v102, v102
	v_exp_f32_e32 v103, v103
	v_exp_f32_e32 v98, v98
	v_exp_f32_e32 v99, v99
	v_pk_mul_f32 v[104:105], v[104:105], v[122:123] op_sel_hi:[1,0]
	v_pk_mul_f32 v[100:101], v[100:101], v[122:123] op_sel_hi:[1,0]
	v_exp_f32_e32 v104, v104
	v_exp_f32_e32 v105, v105
	v_exp_f32_e32 v100, v100
	v_exp_f32_e32 v101, v101
	v_pk_fma_f32 v[102:103], v[120:121], v[102:103], v[120:121] op_sel_hi:[0,1,0]
	v_pk_fma_f32 v[98:99], v[120:121], v[98:99], v[120:121] op_sel_hi:[0,1,0]
	v_rcp_f32_e32 v102, v102
	v_rcp_f32_e32 v103, v103
	v_rcp_f32_e32 v98, v98
	v_rcp_f32_e32 v99, v99
	v_pk_fma_f32 v[104:105], v[120:121], v[104:105], v[120:121] op_sel_hi:[0,1,0]
	v_pk_fma_f32 v[100:101], v[120:121], v[100:101], v[120:121] op_sel_hi:[0,1,0]
	v_rcp_f32_e32 v104, v104
	v_rcp_f32_e32 v105, v105
	v_rcp_f32_e32 v100, v100
	v_rcp_f32_e32 v101, v101
	v_pk_mul_f32 v[102:103], v[110:111], v[102:103]
	v_pk_mul_f32 v[98:99], v[106:107], v[98:99]
	v_med3_f32 v102, v102, s49, v164
	v_med3_f32 v103, v103, s49, v164
	v_med3_f32 v98, v98, s49, v164
	v_med3_f32 v99, v99, s49, v164
	v_cvt_pk_fp8_f32 v116, v102, v103
	v_cvt_pk_fp8_f32 v117, v98, v99
	v_pk_mul_f32 v[104:105], v[112:113], v[104:105]
	v_pk_mul_f32 v[100:101], v[108:109], v[100:101]
	v_med3_f32 v104, v104, s49, v164
	v_med3_f32 v105, v105, s49, v164
	v_med3_f32 v98, v100, s49, v164
	v_med3_f32 v99, v101, s49, v164
	v_cvt_pk_fp8_f32 v116, v104, v105 op_sel:[0,0,1]
	v_cvt_pk_fp8_f32 v117, v98, v99 op_sel:[0,0,1]
	v_ashrrev_i32_e32 v115, 31, v114
	v_lshl_add_u64 v[98:99], v[118:119], 0, v[148:149]
	v_lshl_add_u64 v[100:101], v[114:115], 3, s[10:11]
	global_store_dwordx2 v[98:99], v[116:117], off
	s_nop 0
	s_nop 0
	s_waitcnt vmcnt(7)
	v_mov_b32_e32 v98, v180
	v_mov_b32_e32 v99, v181
	v_ffbh_u32_e32 v101, v99
	v_min_u32_e32 v102, 32, v101
	v_lshlrev_b64 v[98:99], v102, v[98:99]
	v_min_u32_e32 v98, 1, v98
	v_or_b32_e32 v98, v99, v98
	v_cvt_f32_u32_e32 v99, v98
	v_sub_u32_e32 v102, 32, v102
	s_nop 0
	v_or_b32_e32 v98, 48, v152
	v_ldexp_f32 v99, v99, v102
	v_fmamk_f32 v99, v99, 0x30000000, v163
	v_rsq_f32_e32 v105, v99
	v_mul_f32_e32 v104, 0x3e000000, v99
	v_mad_i64_i32 v[102:103], s[26:27], v114, s48, v[150:151]
	v_mul_f32_e32 v106, 0xbfb8aa3b, v105
	v_pk_mul_f32 v[86:87], v[86:87], v[106:107] op_sel_hi:[1,0]
	v_pk_mul_f32 v[82:83], v[82:83], v[106:107] op_sel_hi:[1,0]
	v_exp_f32_e32 v86, v86
	v_exp_f32_e32 v87, v87
	v_exp_f32_e32 v82, v82
	v_exp_f32_e32 v83, v83
	v_pk_mul_f32 v[88:89], v[88:89], v[106:107] op_sel_hi:[1,0]
	v_pk_mul_f32 v[84:85], v[84:85], v[106:107] op_sel_hi:[1,0]
	v_exp_f32_e32 v88, v88
	v_exp_f32_e32 v89, v89
	v_exp_f32_e32 v84, v84
	v_exp_f32_e32 v85, v85
	v_pk_fma_f32 v[86:87], v[104:105], v[86:87], v[104:105] op_sel_hi:[0,1,0]
	v_pk_fma_f32 v[82:83], v[104:105], v[82:83], v[104:105] op_sel_hi:[0,1,0]
	v_rcp_f32_e32 v86, v86
	v_rcp_f32_e32 v87, v87
	v_rcp_f32_e32 v82, v82
	v_rcp_f32_e32 v83, v83
	v_pk_fma_f32 v[88:89], v[104:105], v[88:89], v[104:105] op_sel_hi:[0,1,0]
	v_pk_fma_f32 v[84:85], v[104:105], v[84:85], v[104:105] op_sel_hi:[0,1,0]
	v_rcp_f32_e32 v88, v88
	v_rcp_f32_e32 v89, v89
	v_rcp_f32_e32 v84, v84
	v_rcp_f32_e32 v85, v85
	v_pk_mul_f32 v[86:87], v[94:95], v[86:87]
	v_pk_mul_f32 v[82:83], v[90:91], v[82:83]
	v_med3_f32 v86, v86, s49, v164
	v_med3_f32 v87, v87, s49, v164
	v_med3_f32 v82, v82, s49, v164
	v_med3_f32 v83, v83, s49, v164
	v_cvt_pk_fp8_f32 v100, v86, v87
	v_cvt_pk_fp8_f32 v101, v82, v83
	v_pk_mul_f32 v[88:89], v[96:97], v[88:89]
	v_pk_mul_f32 v[84:85], v[92:93], v[84:85]
	v_med3_f32 v88, v88, s49, v164
	v_med3_f32 v89, v89, s49, v164
	v_med3_f32 v82, v84, s49, v164
	v_med3_f32 v83, v85, s49, v164
	v_cvt_pk_fp8_f32 v100, v88, v89 op_sel:[0,0,1]
	v_cvt_pk_fp8_f32 v101, v82, v83 op_sel:[0,0,1]
	v_ashrrev_i32_e32 v99, 31, v98
	v_lshl_add_u64 v[82:83], v[102:103], 0, v[148:149]
	v_lshl_add_u64 v[84:85], v[98:99], 3, s[10:11]
	global_store_dwordx2 v[82:83], v[100:101], off
	s_nop 0
	s_waitcnt vmcnt(7)
	v_mov_b32_e32 v82, v182
	v_mov_b32_e32 v83, v183
	v_ffbh_u32_e32 v84, v83
	v_min_u32_e32 v84, 32, v84
	v_lshlrev_b64 v[82:83], v84, v[82:83]
	v_min_u32_e32 v82, 1, v82
	v_or_b32_e32 v82, v83, v82
	v_cvt_f32_u32_e32 v82, v82
	v_sub_u32_e32 v83, 32, v84
	v_ldexp_f32 v82, v82, v83
	v_fmamk_f32 v84, v82, 0x30000000, v163
	v_rsq_f32_e32 v85, v84
	v_mul_f32_e32 v84, 0x3e000000, v84
	s_nop 0
	s_nop 0
	v_mul_f32_e32 v86, 0xbfb8aa3b, v85
	v_pk_mul_f32 v[74:75], v[74:75], v[86:87] op_sel_hi:[1,0]
	v_pk_mul_f32 v[70:71], v[70:71], v[86:87] op_sel_hi:[1,0]
	v_exp_f32_e32 v74, v74
	v_exp_f32_e32 v75, v75
	v_exp_f32_e32 v70, v70
	v_exp_f32_e32 v71, v71
	v_pk_mul_f32 v[76:77], v[76:77], v[86:87] op_sel_hi:[1,0]
	v_pk_mul_f32 v[72:73], v[72:73], v[86:87] op_sel_hi:[1,0]
	v_exp_f32_e32 v76, v76
	v_exp_f32_e32 v77, v77
	v_exp_f32_e32 v72, v72
	v_exp_f32_e32 v73, v73
	v_pk_fma_f32 v[74:75], v[84:85], v[74:75], v[84:85] op_sel_hi:[0,1,0]
	v_pk_fma_f32 v[70:71], v[84:85], v[70:71], v[84:85] op_sel_hi:[0,1,0]
	v_rcp_f32_e32 v74, v74
	v_rcp_f32_e32 v75, v75
	v_rcp_f32_e32 v70, v70
	v_rcp_f32_e32 v71, v71
	v_pk_fma_f32 v[76:77], v[84:85], v[76:77], v[84:85] op_sel_hi:[0,1,0]
	v_pk_fma_f32 v[72:73], v[84:85], v[72:73], v[84:85] op_sel_hi:[0,1,0]
	v_rcp_f32_e32 v76, v76
	v_rcp_f32_e32 v77, v77
	v_rcp_f32_e32 v72, v72
	v_rcp_f32_e32 v73, v73
	v_pk_mul_f32 v[74:75], v[78:79], v[74:75]
	v_pk_mul_f32 v[66:67], v[66:67], v[70:71]
	v_med3_f32 v70, v74, s49, v164
	v_med3_f32 v71, v75, s49, v164
	v_med3_f32 v66, v66, s49, v164
	v_med3_f32 v67, v67, s49, v164
	v_cvt_pk_fp8_f32 v82, v70, v71
	v_cvt_pk_fp8_f32 v83, v66, v67
	v_pk_mul_f32 v[76:77], v[80:81], v[76:77]
	v_pk_mul_f32 v[68:69], v[68:69], v[72:73]
	v_med3_f32 v72, v76, s49, v164
	v_med3_f32 v73, v77, s49, v164
	v_med3_f32 v66, v68, s49, v164
	v_med3_f32 v67, v69, s49, v164
	v_cvt_pk_fp8_f32 v82, v72, v73 op_sel:[0,0,1]
	v_cvt_pk_fp8_f32 v83, v66, v67 op_sel:[0,0,1]
	v_mad_i64_i32 v[66:67], s[26:27], v98, s48, v[150:151]
	v_lshl_add_u64 v[66:67], v[66:67], 0, v[148:149]
	global_store_dwordx2 v[66:67], v[82:83], off
	s_nop 0
	v_add_u32_e32 v71, 0x80, v152
	s_waitcnt vmcnt(7)
	v_mov_b32_e32 v66, v184
	v_mov_b32_e32 v67, v185
	v_ffbh_u32_e32 v68, v67
	v_min_u32_e32 v68, 32, v68
	v_lshlrev_b64 v[66:67], v68, v[66:67]
	v_min_u32_e32 v66, 1, v66
	v_or_b32_e32 v66, v67, v66
	v_cvt_f32_u32_e32 v67, v66
	v_sub_u32_e32 v68, 32, v68
	s_nop 0
	v_ldexp_f32 v67, v67, v68
	v_fmamk_f32 v68, v67, 0x30000000, v163
	v_rsq_f32_e32 v69, v68
	v_mul_f32_e32 v68, 0x3e000000, v68
	s_nop 0
	v_mul_f32_e32 v70, 0xbfb8aa3b, v69
	v_pk_mul_f32 v[58:59], v[58:59], v[70:71] op_sel_hi:[1,0]
	v_pk_mul_f32 v[54:55], v[54:55], v[70:71] op_sel_hi:[1,0]
	v_exp_f32_e32 v58, v58
	v_exp_f32_e32 v59, v59
	v_exp_f32_e32 v54, v54
	v_exp_f32_e32 v55, v55
	v_pk_mul_f32 v[60:61], v[60:61], v[70:71] op_sel_hi:[1,0]
	v_pk_mul_f32 v[56:57], v[56:57], v[70:71] op_sel_hi:[1,0]
	v_exp_f32_e32 v60, v60
	v_exp_f32_e32 v61, v61
	v_exp_f32_e32 v56, v56
	v_exp_f32_e32 v57, v57
	v_pk_fma_f32 v[58:59], v[68:69], v[58:59], v[68:69] op_sel_hi:[0,1,0]
	v_pk_fma_f32 v[54:55], v[68:69], v[54:55], v[68:69] op_sel_hi:[0,1,0]
	v_rcp_f32_e32 v58, v58
	v_rcp_f32_e32 v59, v59
	v_rcp_f32_e32 v54, v54
	v_rcp_f32_e32 v55, v55
	v_pk_fma_f32 v[60:61], v[68:69], v[60:61], v[68:69] op_sel_hi:[0,1,0]
	v_pk_fma_f32 v[56:57], v[68:69], v[56:57], v[68:69] op_sel_hi:[0,1,0]
	v_rcp_f32_e32 v60, v60
	v_rcp_f32_e32 v61, v61
	v_rcp_f32_e32 v56, v56
	v_rcp_f32_e32 v57, v57
	v_pk_mul_f32 v[58:59], v[62:63], v[58:59]
	v_pk_mul_f32 v[50:51], v[50:51], v[54:55]
	v_med3_f32 v54, v58, s49, v164
	v_med3_f32 v55, v59, s49, v164
	v_med3_f32 v50, v50, s49, v164
	v_med3_f32 v51, v51, s49, v164
	v_cvt_pk_fp8_f32 v66, v54, v55
	v_cvt_pk_fp8_f32 v67, v50, v51
	v_pk_mul_f32 v[60:61], v[64:65], v[60:61]
	v_pk_mul_f32 v[52:53], v[52:53], v[56:57]
	v_med3_f32 v56, v60, s49, v164
	v_med3_f32 v57, v61, s49, v164
	v_med3_f32 v50, v52, s49, v164
	v_med3_f32 v51, v53, s49, v164
	v_cvt_pk_fp8_f32 v66, v56, v57 op_sel:[0,0,1]
	v_cvt_pk_fp8_f32 v67, v50, v51 op_sel:[0,0,1]
	v_mad_i64_i32 v[50:51], s[26:27], v71, s48, v[150:151]
	v_lshl_add_u64 v[50:51], v[50:51], 0, v[148:149]
	global_store_dwordx2 v[50:51], v[66:67], off
	s_nop 0
	v_add_u32_e32 v55, 0x90, v152
	s_waitcnt vmcnt(7)
	v_mov_b32_e32 v50, v186
	v_mov_b32_e32 v51, v187
	v_ffbh_u32_e32 v52, v51
	v_min_u32_e32 v52, 32, v52
	v_lshlrev_b64 v[50:51], v52, v[50:51]
	v_min_u32_e32 v50, 1, v50
	v_or_b32_e32 v50, v51, v50
	v_cvt_f32_u32_e32 v51, v50
	v_sub_u32_e32 v52, 32, v52
	s_nop 0
	v_ldexp_f32 v51, v51, v52
	v_fmamk_f32 v52, v51, 0x30000000, v163
	v_rsq_f32_e32 v53, v52
	v_mul_f32_e32 v52, 0x3e000000, v52
	s_nop 0
	v_mul_f32_e32 v54, 0xbfb8aa3b, v53
	v_pk_mul_f32 v[42:43], v[42:43], v[54:55] op_sel_hi:[1,0]
	v_pk_mul_f32 v[38:39], v[38:39], v[54:55] op_sel_hi:[1,0]
	v_exp_f32_e32 v42, v42
	v_exp_f32_e32 v43, v43
	v_exp_f32_e32 v38, v38
	v_exp_f32_e32 v39, v39
	v_pk_mul_f32 v[44:45], v[44:45], v[54:55] op_sel_hi:[1,0]
	v_pk_mul_f32 v[40:41], v[40:41], v[54:55] op_sel_hi:[1,0]
	v_exp_f32_e32 v44, v44
	v_exp_f32_e32 v45, v45
	v_exp_f32_e32 v40, v40
	v_exp_f32_e32 v41, v41
	v_pk_fma_f32 v[42:43], v[52:53], v[42:43], v[52:53] op_sel_hi:[0,1,0]
	v_pk_fma_f32 v[38:39], v[52:53], v[38:39], v[52:53] op_sel_hi:[0,1,0]
	v_rcp_f32_e32 v42, v42
	v_rcp_f32_e32 v43, v43
	v_rcp_f32_e32 v38, v38
	v_rcp_f32_e32 v39, v39
	v_pk_fma_f32 v[44:45], v[52:53], v[44:45], v[52:53] op_sel_hi:[0,1,0]
	v_pk_fma_f32 v[40:41], v[52:53], v[40:41], v[52:53] op_sel_hi:[0,1,0]
	v_rcp_f32_e32 v44, v44
	v_rcp_f32_e32 v45, v45
	v_rcp_f32_e32 v40, v40
	v_rcp_f32_e32 v41, v41
	v_pk_mul_f32 v[42:43], v[46:47], v[42:43]
	v_pk_mul_f32 v[34:35], v[34:35], v[38:39]
	v_med3_f32 v38, v42, s49, v164
	v_med3_f32 v39, v43, s49, v164
	v_med3_f32 v34, v34, s49, v164
	v_med3_f32 v35, v35, s49, v164
	v_cvt_pk_fp8_f32 v50, v38, v39
	v_cvt_pk_fp8_f32 v51, v34, v35
	v_pk_mul_f32 v[44:45], v[48:49], v[44:45]
	v_pk_mul_f32 v[36:37], v[36:37], v[40:41]
	v_med3_f32 v40, v44, s49, v164
	v_med3_f32 v41, v45, s49, v164
	v_med3_f32 v34, v36, s49, v164
	v_med3_f32 v35, v37, s49, v164
	v_cvt_pk_fp8_f32 v50, v40, v41 op_sel:[0,0,1]
	v_cvt_pk_fp8_f32 v51, v34, v35 op_sel:[0,0,1]
	v_mad_i64_i32 v[34:35], s[26:27], v55, s48, v[150:151]
	v_lshl_add_u64 v[34:35], v[34:35], 0, v[148:149]
	global_store_dwordx2 v[34:35], v[50:51], off
	s_nop 0
	v_add_u32_e32 v39, 0xa0, v152
	s_waitcnt vmcnt(7)
	v_mov_b32_e32 v34, v188
	v_mov_b32_e32 v35, v189
	v_ffbh_u32_e32 v36, v35
	v_min_u32_e32 v36, 32, v36
	v_lshlrev_b64 v[34:35], v36, v[34:35]
	v_min_u32_e32 v34, 1, v34
	v_or_b32_e32 v34, v35, v34
	v_cvt_f32_u32_e32 v35, v34
	v_sub_u32_e32 v36, 32, v36
	s_nop 0
	v_ldexp_f32 v35, v35, v36
	v_fmamk_f32 v36, v35, 0x30000000, v163
	v_rsq_f32_e32 v37, v36
	v_mul_f32_e32 v36, 0x3e000000, v36
	s_nop 0
	v_mul_f32_e32 v38, 0xbfb8aa3b, v37
	v_pk_mul_f32 v[26:27], v[26:27], v[38:39] op_sel_hi:[1,0]
	v_pk_mul_f32 v[22:23], v[22:23], v[38:39] op_sel_hi:[1,0]
	v_exp_f32_e32 v26, v26
	v_exp_f32_e32 v27, v27
	v_exp_f32_e32 v22, v22
	v_exp_f32_e32 v23, v23
	v_pk_mul_f32 v[28:29], v[28:29], v[38:39] op_sel_hi:[1,0]
	v_pk_mul_f32 v[24:25], v[24:25], v[38:39] op_sel_hi:[1,0]
	v_exp_f32_e32 v28, v28
	v_exp_f32_e32 v29, v29
	v_exp_f32_e32 v24, v24
	v_exp_f32_e32 v25, v25
	v_pk_fma_f32 v[26:27], v[36:37], v[26:27], v[36:37] op_sel_hi:[0,1,0]
	v_pk_fma_f32 v[22:23], v[36:37], v[22:23], v[36:37] op_sel_hi:[0,1,0]
	v_rcp_f32_e32 v26, v26
	v_rcp_f32_e32 v27, v27
	v_rcp_f32_e32 v22, v22
	v_rcp_f32_e32 v23, v23
	v_pk_fma_f32 v[28:29], v[36:37], v[28:29], v[36:37] op_sel_hi:[0,1,0]
	v_pk_fma_f32 v[24:25], v[36:37], v[24:25], v[36:37] op_sel_hi:[0,1,0]
	v_rcp_f32_e32 v28, v28
	v_rcp_f32_e32 v29, v29
	v_rcp_f32_e32 v24, v24
	v_rcp_f32_e32 v25, v25
	v_pk_mul_f32 v[26:27], v[30:31], v[26:27]
	v_pk_mul_f32 v[18:19], v[18:19], v[22:23]
	v_med3_f32 v22, v26, s49, v164
	v_med3_f32 v23, v27, s49, v164
	v_med3_f32 v18, v18, s49, v164
	v_med3_f32 v19, v19, s49, v164
	v_cvt_pk_fp8_f32 v34, v22, v23
	v_cvt_pk_fp8_f32 v35, v18, v19
	v_pk_mul_f32 v[28:29], v[32:33], v[28:29]
	v_pk_mul_f32 v[20:21], v[20:21], v[24:25]
	v_med3_f32 v24, v28, s49, v164
	v_med3_f32 v25, v29, s49, v164
	v_med3_f32 v18, v20, s49, v164
	v_med3_f32 v19, v21, s49, v164
	v_cvt_pk_fp8_f32 v34, v24, v25 op_sel:[0,0,1]
	v_cvt_pk_fp8_f32 v35, v18, v19 op_sel:[0,0,1]
	v_mad_i64_i32 v[18:19], s[26:27], v39, s48, v[150:151]
	v_lshl_add_u64 v[18:19], v[18:19], 0, v[148:149]
	global_store_dwordx2 v[18:19], v[34:35], off
	s_nop 0
	v_add_u32_e32 v23, 0xb0, v152
	s_nop 0
	s_waitcnt vmcnt(7)
	v_mov_b32_e32 v18, v190
	v_mov_b32_e32 v19, v191
	v_ffbh_u32_e32 v21, v19
	v_min_u32_e32 v22, 32, v21
	v_lshlrev_b64 v[18:19], v22, v[18:19]
	v_min_u32_e32 v18, 1, v18
	v_or_b32_e32 v18, v19, v18
	v_cvt_f32_u32_e32 v18, v18
	v_sub_u32_e32 v19, 32, v22
	s_nop 0
	v_ldexp_f32 v18, v18, v19
	v_fmamk_f32 v18, v18, 0x30000000, v163
	v_rsq_f32_e32 v19, v18
	v_mul_f32_e32 v18, 0x3e000000, v18
	v_mul_f32_e32 v22, 0xbfb8aa3b, v19
	v_pk_mul_f32 v[6:7], v[6:7], v[22:23] op_sel_hi:[1,0]
	v_pk_mul_f32 v[2:3], v[2:3], v[22:23] op_sel_hi:[1,0]
	v_exp_f32_e32 v6, v6
	v_exp_f32_e32 v7, v7
	v_exp_f32_e32 v2, v2
	v_exp_f32_e32 v3, v3
	v_pk_mul_f32 v[8:9], v[8:9], v[22:23] op_sel_hi:[1,0]
	v_pk_mul_f32 v[4:5], v[4:5], v[22:23] op_sel_hi:[1,0]
	v_exp_f32_e32 v8, v8
	v_exp_f32_e32 v9, v9
	v_exp_f32_e32 v4, v4
	v_exp_f32_e32 v5, v5
	v_pk_fma_f32 v[6:7], v[18:19], v[6:7], v[18:19] op_sel_hi:[0,1,0]
	v_pk_fma_f32 v[2:3], v[18:19], v[2:3], v[18:19] op_sel_hi:[0,1,0]
	v_rcp_f32_e32 v6, v6
	v_rcp_f32_e32 v7, v7
	v_rcp_f32_e32 v2, v2
	v_rcp_f32_e32 v3, v3
	v_pk_fma_f32 v[8:9], v[18:19], v[8:9], v[18:19] op_sel_hi:[0,1,0]
	v_pk_fma_f32 v[4:5], v[18:19], v[4:5], v[18:19] op_sel_hi:[0,1,0]
	v_rcp_f32_e32 v8, v8
	v_rcp_f32_e32 v9, v9
	v_rcp_f32_e32 v4, v4
	v_rcp_f32_e32 v5, v5
	v_pk_mul_f32 v[6:7], v[14:15], v[6:7]
	v_pk_mul_f32 v[2:3], v[10:11], v[2:3]
	v_med3_f32 v6, v6, s49, v164
	v_med3_f32 v7, v7, s49, v164
	v_med3_f32 v2, v2, s49, v164
	v_med3_f32 v3, v3, s49, v164
	v_cvt_pk_fp8_f32 v20, v6, v7
	v_cvt_pk_fp8_f32 v21, v2, v3
	v_pk_mul_f32 v[8:9], v[16:17], v[8:9]
	v_pk_mul_f32 v[4:5], v[12:13], v[4:5]
	v_med3_f32 v8, v8, s49, v164
	v_med3_f32 v9, v9, s49, v164
	v_med3_f32 v2, v4, s49, v164
	v_med3_f32 v3, v5, s49, v164
	v_cvt_pk_fp8_f32 v20, v8, v9 op_sel:[0,0,1]
	v_cvt_pk_fp8_f32 v21, v2, v3 op_sel:[0,0,1]
	v_mad_i64_i32 v[2:3], s[26:27], v23, s48, v[150:151]
	v_lshl_add_u64 v[2:3], v[2:3], 0, v[148:149]
	global_store_dwordx2 v[2:3], v[20:21], off
	s_cbranch_vccnz .LBB0_467
	s_andn2_b64 vcc, exec, s[6:7]
	s_cbranch_vccnz .LBB0_466
	s_barrier
	s_branch .LBB0_466

.LBB0_918:
	s_waitcnt vmcnt(14)
	v_mov_b64_e32 v[116:117], v[20:21]
	v_mov_b64_e32 v[124:125], v[12:13]
	v_mov_b64_e32 v[114:115], v[18:19]
	v_mov_b64_e32 v[122:123], v[10:11]
	v_mov_b32_e32 v196, v125
	v_mov_b32_e32 v197, v117
	v_mov_b32_e32 v192, v123
	v_mov_b32_e32 v193, v115
	v_mov_b32_e32 v194, v124
	v_mov_b32_e32 v195, v116
	v_pk_mul_f32 v[196:197], v[196:197], v[196:197]
	s_waitcnt vmcnt(12)
	v_mov_b64_e32 v[120:121], v[16:17]
	v_mov_b64_e32 v[128:129], v[8:9]
	v_pk_mul_f32 v[192:193], v[192:193], v[192:193]
	v_pk_fma_f32 v[194:195], v[194:195], v[194:195], v[196:197]
	v_mov_b32_e32 v196, v122
	v_mov_b32_e32 v197, v114
	s_waitcnt vmcnt(11)
	v_mov_b64_e32 v[108:109], v[32:33]
	v_mov_b64_e32 v[118:119], v[14:15]
	v_mov_b64_e32 v[126:127], v[6:7]
	v_pk_fma_f32 v[192:193], v[196:197], v[196:197], v[192:193]
	v_mov_b32_e32 v198, v129
	v_mov_b32_e32 v199, v121
	s_waitcnt vmcnt(10)
	v_mov_b64_e32 v[100:101], v[40:41]
	v_mov_b64_e32 v[106:107], v[30:31]
	v_pk_add_f32 v[192:193], v[192:193], v[194:195]
	v_mov_b32_e32 v194, v127
	v_mov_b32_e32 v195, v119
	v_mov_b32_e32 v196, v128
	v_mov_b32_e32 v197, v120
	v_pk_mul_f32 v[198:199], v[198:199], v[198:199]
	v_mov_b64_e32 v[98:99], v[38:39]
	v_pk_mul_f32 v[6:7], v[108:109], v[108:109]
	v_pk_mul_f32 v[8:9], v[106:107], v[106:107]
	v_pk_mul_f32 v[194:195], v[194:195], v[194:195]
	v_pk_fma_f32 v[196:197], v[196:197], v[196:197], v[198:199]
	v_mov_b32_e32 v198, v126
	v_mov_b32_e32 v199, v118
	s_waitcnt vmcnt(7)
	v_mov_b64_e32 v[96:97], v[48:49]
	v_mov_b64_e32 v[112:113], v[24:25]
	v_pk_mov_b32 v[10:11], v[8:9], v[6:7] op_sel:[1,0]
	v_mov_b32_e32 v9, v7
	v_pk_fma_f32 v[194:195], v[198:199], v[198:199], v[194:195]
	v_mul_f32_e32 v138, v99, v99
	v_mov_b64_e32 v[94:95], v[46:47]
	v_mov_b64_e32 v[104:105], v[28:29]
	v_mov_b64_e32 v[110:111], v[22:23]
	v_pk_add_f32 v[130:131], v[10:11], v[8:9]
	v_pk_add_f32 v[194:195], v[194:195], v[196:197]
	v_pk_fma_f32 v[196:197], v[98:99], v[98:99], v[138:139] op_sel_hi:[1,1,0]
	v_mul_f32_e32 v138, v101, v101
	v_mov_b64_e32 v[102:103], v[26:27]
	v_pk_mul_f32 v[6:7], v[112:113], v[112:113]
	v_pk_mul_f32 v[8:9], v[110:111], v[110:111]
	v_mul_f32_e32 v162, v94, v94
	v_mul_f32_e32 v200, v95, v95
	v_mul_f32_e32 v201, v96, v96
	v_mul_f32_e32 v202, v97, v97
	v_pk_fma_f32 v[198:199], v[100:101], v[100:101], v[138:139] op_sel_hi:[1,1,0]
	v_pk_add_f32 v[192:193], v[192:193], v[192:193] op_sel:[0,1] op_sel_hi:[1,0]
	v_pk_add_f32 v[130:131], v[130:131], v[130:131] op_sel:[0,1] op_sel_hi:[1,0]
	s_waitcnt vmcnt(6)
	v_mov_b64_e32 v[92:93], v[36:37]
	v_pk_mov_b32 v[10:11], v[8:9], v[6:7] op_sel:[1,0]
	v_mov_b32_e32 v9, v7
	v_mov_b32_e32 v197, v201
	v_mov_b32_e32 v199, v202
	v_mov_b32_e32 v193, v162
	v_mov_b32_e32 v131, v200
	v_mul_f32_e32 v138, v103, v103
	s_waitcnt vmcnt(5)
	v_mov_b64_e32 v[84:85], v[56:57]
	v_mov_b64_e32 v[90:91], v[34:35]
	v_pk_add_f32 v[132:133], v[10:11], v[8:9]
	v_pk_add_f32 v[196:197], v[196:197], v[198:199]
	v_pk_add_f32 v[130:131], v[192:193], v[130:131]
	v_pk_fma_f32 v[192:193], v[102:103], v[102:103], v[138:139] op_sel_hi:[1,1,0]
	v_mul_f32_e32 v138, v105, v105
	s_waitcnt vmcnt(3)
	v_mov_b64_e32 v[76:77], v[64:65]
	v_mov_b64_e32 v[82:83], v[54:55]
	v_mul_f32_e32 v203, v90, v90
	v_mul_f32_e32 v204, v91, v91
	v_mul_f32_e32 v205, v92, v92
	v_mul_f32_e32 v206, v93, v93
	v_pk_add_f32 v[130:131], v[130:131], v[196:197]
	v_pk_fma_f32 v[196:197], v[104:105], v[104:105], v[138:139] op_sel_hi:[1,1,0]
	v_pk_add_f32 v[194:195], v[194:195], v[194:195] op_sel:[0,1] op_sel_hi:[1,0]
	v_pk_add_f32 v[132:133], v[132:133], v[132:133] op_sel:[0,1] op_sel_hi:[1,0]
	v_mov_b64_e32 v[74:75], v[62:63]
	v_pk_mul_f32 v[6:7], v[84:85], v[84:85]
	v_pk_mul_f32 v[8:9], v[82:83], v[82:83]
	v_mov_b32_e32 v193, v205
	v_mov_b32_e32 v197, v206
	v_mov_b32_e32 v195, v203
	v_mov_b32_e32 v133, v204
	v_mov_b64_e32 v[88:89], v[44:45]
	v_pk_mov_b32 v[10:11], v[8:9], v[6:7] op_sel:[1,0]
	v_mov_b32_e32 v9, v7
	s_waitcnt vmcnt(1)
	v_mov_b64_e32 v[72:73], v[4:5]
	v_pk_add_f32 v[192:193], v[192:193], v[196:197]
	v_pk_add_f32 v[132:133], v[194:195], v[132:133]
	v_mul_f32_e32 v138, v75, v75
	v_mov_b64_e32 v[80:81], v[52:53]
	v_mov_b64_e32 v[86:87], v[42:43]
	v_pk_add_f32 v[188:189], v[10:11], v[8:9]
	v_mov_b64_e32 v[70:71], v[2:3]
	v_pk_add_f32 v[132:133], v[132:133], v[192:193]
	v_pk_fma_f32 v[192:193], v[74:75], v[74:75], v[138:139] op_sel_hi:[1,1,0]
	v_mul_f32_e32 v138, v77, v77
	v_mov_b64_e32 v[78:79], v[50:51]
	v_pk_mul_f32 v[6:7], v[88:89], v[88:89]
	v_pk_mul_f32 v[8:9], v[86:87], v[86:87]
	v_mul_f32_e32 v207, v70, v70
	v_mul_f32_e32 v208, v71, v71
	v_mul_f32_e32 v209, v72, v72
	v_mul_f32_e32 v210, v73, v73
	v_pk_fma_f32 v[194:195], v[76:77], v[76:77], v[138:139] op_sel_hi:[1,1,0]
	v_pk_add_f32 v[130:131], v[130:131], v[130:131] op_sel:[0,1] op_sel_hi:[1,0]
	v_pk_add_f32 v[188:189], v[188:189], v[188:189] op_sel:[0,1] op_sel_hi:[1,0]
	s_waitcnt vmcnt(0)
	v_mov_b64_e32 v[68:69], v[60:61]
	v_pk_mov_b32 v[10:11], v[8:9], v[6:7] op_sel:[1,0]
	v_mov_b32_e32 v9, v7
	v_mov_b32_e32 v193, v209
	v_mov_b32_e32 v195, v210
	v_mov_b32_e32 v131, v207
	v_mov_b32_e32 v189, v208
	v_mul_f32_e32 v138, v79, v79
	v_mov_b64_e32 v[66:67], v[58:59]
	v_pk_add_f32 v[190:191], v[10:11], v[8:9]
	v_pk_add_f32 v[192:193], v[192:193], v[194:195]
	v_pk_add_f32 v[130:131], v[130:131], v[188:189]
	v_pk_fma_f32 v[188:189], v[78:79], v[78:79], v[138:139] op_sel_hi:[1,1,0]
	v_mul_f32_e32 v138, v81, v81
	v_mul_f32_e32 v211, v66, v66
	v_mul_f32_e32 v212, v67, v67
	v_mul_f32_e32 v213, v68, v68
	v_mul_f32_e32 v214, v69, v69
	v_pk_add_f32 v[130:131], v[130:131], v[192:193]
	v_pk_fma_f32 v[192:193], v[80:81], v[80:81], v[138:139] op_sel_hi:[1,1,0]
	v_pk_add_f32 v[132:133], v[132:133], v[132:133] op_sel:[0,1] op_sel_hi:[1,0]
	v_pk_add_f32 v[190:191], v[190:191], v[190:191] op_sel:[0,1] op_sel_hi:[1,0]
	v_mov_b32_e32 v189, v213
	v_mov_b32_e32 v193, v214
	v_mov_b32_e32 v133, v211
	v_mov_b32_e32 v191, v212
	v_pk_add_f32 v[188:189], v[188:189], v[192:193]
	v_pk_add_f32 v[132:133], v[132:133], v[190:191]
	v_add_f32_e32 v130, v130, v131
	v_pk_add_f32 v[132:133], v[132:133], v[188:189]
	s_cmp_eq_u32 s37, 24
	v_add_f32_e32 v131, v132, v133
	ds_bpermute_b32 v132, v1, v130
	s_cselect_b32 s0, 0, 2
	s_add_u32 s0, s0, s62
	s_addc_u32 s1, 0, s63
	s_lshl_b64 s[0:1], s[0:1], 13
	s_waitcnt lgkmcnt(0)
	v_add_f32_e32 v130, v130, v132
	ds_bpermute_b32 v132, v1, v131
	s_add_u32 s0, s28, s0
	s_addc_u32 s1, s29, s1
	s_add_u32 s14, s0, 0x2000
	s_addc_u32 s15, s1, 0
	s_waitcnt lgkmcnt(0)
	v_add_f32_e32 v131, v131, v132
	ds_bpermute_b32 v132, v135, v130
	global_load_dwordx4 v[10:13], v178, s[0:1]
	global_load_dwordx4 v[6:9], v178, s[14:15]
	global_load_dwordx4 v[18:21], v178, s[0:1] offset:1024
	global_load_dwordx4 v[14:17], v168, s[14:15]
	global_load_dwordx4 v[30:33], v178, s[0:1] offset:2048
	global_load_dwordx4 v[22:25], v169, s[14:15]
	global_load_dwordx4 v[38:41], v178, s[0:1] offset:3072
	global_load_dwordx4 v[26:29], v170, s[14:15]
	global_load_dwordx4 v[46:49], v171, s[0:1]
	global_load_dwordx4 v[34:37], v171, s[14:15]
	global_load_dwordx4 v[54:57], v172, s[0:1]
	global_load_dwordx4 v[42:45], v172, s[14:15]
	global_load_dwordx4 v[62:65], v173, s[0:1]
	global_load_dwordx4 v[50:53], v173, s[14:15]
	global_load_dwordx4 v[2:5], v174, s[0:1]
	global_load_dwordx4 v[58:61], v174, s[14:15]
	s_waitcnt lgkmcnt(0)
	v_add_f32_e32 v130, v130, v132
	ds_bpermute_b32 v132, v135, v131
	s_waitcnt lgkmcnt(0)
	v_add_f32_e32 v131, v131, v132
	ds_bpermute_b32 v132, v137, v130
	s_waitcnt lgkmcnt(0)
	v_add_f32_e32 v130, v130, v132
	ds_bpermute_b32 v132, v137, v131
	s_waitcnt lgkmcnt(0)
	v_add_f32_e32 v131, v131, v132
	ds_bpermute_b32 v132, v147, v130
	s_waitcnt lgkmcnt(0)
	v_add_f32_e32 v130, v130, v132
	ds_bpermute_b32 v132, v147, v131
	s_waitcnt lgkmcnt(0)
	v_add_f32_e32 v131, v131, v132
	ds_bpermute_b32 v132, v164, v130
	s_waitcnt lgkmcnt(0)
	v_add_f32_e32 v130, v130, v132
	ds_bpermute_b32 v132, v164, v131
	s_waitcnt lgkmcnt(0)
	v_add_f32_e32 v131, v131, v132
	ds_bpermute_b32 v132, v165, v130
	s_waitcnt lgkmcnt(0)
	v_add_f32_e32 v130, v130, v132
	ds_bpermute_b32 v132, v165, v131
	v_fmamk_f32 v130, v130, 0x3a000000, v175
	v_cmp_gt_f32_e32 vcc, s3, v130
	s_waitcnt lgkmcnt(0)
	v_add_f32_e32 v131, v131, v132
	v_mul_f32_e32 v132, 0x4f800000, v130
	v_cndmask_b32_e32 v130, v130, v132, vcc
	v_sqrt_f32_e32 v132, v130
	s_nop 0
	v_add_u32_e32 v133, -1, v132
	v_fma_f32 v138, -v133, v132, v130
	v_cmp_ge_f32_e64 s[0:1], 0, v138
	v_add_u32_e32 v138, 1, v132
	s_nop 0
	v_cndmask_b32_e64 v133, v132, v133, s[0:1]
	v_fma_f32 v132, -v138, v132, v130
	v_cmp_lt_f32_e64 s[0:1], 0, v132
	s_nop 1
	v_cndmask_b32_e64 v132, v133, v138, s[0:1]
	v_mul_f32_e32 v133, 0x37800000, v132
	v_cndmask_b32_e32 v132, v132, v133, vcc
	v_cmp_class_f32_e32 vcc, v130, v176
	s_nop 1
	v_cndmask_b32_e32 v130, v132, v130, vcc
	v_div_scale_f32 v132, s[0:1], v130, v130, 1.0
	v_rcp_f32_e32 v133, v132
	s_nop 0
	v_fma_f32 v138, -v132, v133, 1.0
	v_fmac_f32_e32 v133, v138, v133
	v_div_scale_f32 v138, vcc, 1.0, v130, 1.0
	v_mul_f32_e32 v162, v138, v133
	v_fma_f32 v188, -v132, v162, v138
	v_fmac_f32_e32 v162, v188, v133
	v_fma_f32 v132, -v132, v162, v138
	v_div_fmas_f32 v132, v132, v133, v162
	v_div_fixup_f32 v162, v132, v130, 1.0
	v_fmamk_f32 v130, v131, 0x3a000000, v175
	v_cmp_gt_f32_e32 vcc, s3, v130
	v_mul_f32_e32 v131, 0x4f800000, v130
	v_pk_mul_f32 v[122:123], v[122:123], v[162:163] op_sel_hi:[1,0]
	v_cndmask_b32_e32 v130, v130, v131, vcc
	v_sqrt_f32_e32 v131, v130
	v_pk_mul_f32 v[124:125], v[124:125], v[162:163] op_sel_hi:[1,0]
	v_pk_mul_f32 v[114:115], v[114:115], v[162:163] op_sel_hi:[1,0]
	v_pk_mul_f32 v[116:117], v[116:117], v[162:163] op_sel_hi:[1,0]
	v_add_u32_e32 v132, -1, v131
	v_fma_f32 v133, -v132, v131, v130
	v_cmp_ge_f32_e64 s[0:1], 0, v133
	v_add_u32_e32 v133, 1, v131
	v_pk_mul_f32 v[106:107], v[106:107], v[162:163] op_sel_hi:[1,0]
	v_cndmask_b32_e64 v132, v131, v132, s[0:1]
	v_fma_f32 v131, -v133, v131, v130
	v_cmp_lt_f32_e64 s[0:1], 0, v131
	v_pk_mul_f32 v[108:109], v[108:109], v[162:163] op_sel_hi:[1,0]
	v_pk_mul_f32 v[98:99], v[98:99], v[162:163] op_sel_hi:[1,0]
	v_cndmask_b32_e64 v131, v132, v133, s[0:1]
	v_mul_f32_e32 v132, 0x37800000, v131
	v_cndmask_b32_e32 v131, v131, v132, vcc
	v_cmp_class_f32_e32 vcc, v130, v176
	v_pk_mul_f32 v[100:101], v[100:101], v[162:163] op_sel_hi:[1,0]
	v_pk_mul_f32 v[82:83], v[82:83], v[162:163] op_sel_hi:[1,0]
	v_cndmask_b32_e32 v130, v131, v130, vcc
	v_div_scale_f32 v131, s[0:1], v130, v130, 1.0
	v_rcp_f32_e32 v132, v131
	v_pk_mul_f32 v[84:85], v[84:85], v[162:163] op_sel_hi:[1,0]
	v_pk_mul_f32 v[74:75], v[74:75], v[162:163] op_sel_hi:[1,0]
	v_pk_mul_f32 v[76:77], v[76:77], v[162:163] op_sel_hi:[1,0]
	v_fma_f32 v133, -v131, v132, 1.0
	v_fmac_f32_e32 v132, v133, v132
	v_div_scale_f32 v133, vcc, 1.0, v130, 1.0
	v_mul_f32_e32 v138, v133, v132
	v_fma_f32 v188, -v131, v138, v133
	v_fmac_f32_e32 v138, v188, v132
	v_fma_f32 v131, -v131, v138, v133
	v_div_fmas_f32 v131, v131, v132, v138
	v_div_fixup_f32 v138, v131, v130, 1.0
	global_load_dwordx4 v[130:133], v[140:141], off
	v_pk_mul_f32 v[92:93], v[92:93], v[138:139] op_sel_hi:[1,0]
	v_pk_mul_f32 v[90:91], v[90:91], v[138:139] op_sel_hi:[1,0]
	v_pk_mul_f32 v[70:71], v[70:71], v[162:163] op_sel_hi:[1,0]
	v_pk_mul_f32 v[66:67], v[66:67], v[138:139] op_sel_hi:[1,0]
	v_pk_mul_f32 v[72:73], v[72:73], v[162:163] op_sel_hi:[1,0]
	v_pk_mul_f32 v[68:69], v[68:69], v[138:139] op_sel_hi:[1,0]
	s_waitcnt vmcnt(0)
	v_pk_mul_f32 v[190:191], v[130:131], v[122:123]
	v_pk_mul_f32 v[122:123], v[126:127], v[138:139] op_sel_hi:[1,0]
	s_nop 0
	v_pk_mul_f32 v[192:193], v[130:131], v[122:123]
	v_med3_f32 v122, v190, s78, v179
	v_med3_f32 v123, v191, s78, v179
	v_cvt_pk_fp8_f32 v126, v122, v123
	v_pk_mul_f32 v[188:189], v[132:133], v[124:125]
	v_pk_mul_f32 v[124:125], v[128:129], v[138:139] op_sel_hi:[1,0]
	s_nop 0
	v_pk_mul_f32 v[132:133], v[132:133], v[124:125]
	v_med3_f32 v124, v188, s78, v179
	v_med3_f32 v125, v189, s78, v179
	v_cvt_pk_fp8_f32 v126, v124, v125 op_sel:[0,0,1]
	v_med3_f32 v124, v192, s78, v179
	v_med3_f32 v125, v193, s78, v179
	v_cvt_pk_fp8_f32 v128, v124, v125
	v_lshl_add_u64 v[122:123], s[46:47], 0, v[160:161]
	global_store_dword v[122:123], v126, off offset:-2048
	v_med3_f32 v126, v132, s78, v179
	v_med3_f32 v127, v133, s78, v179
	v_cvt_pk_fp8_f32 v128, v126, v127 op_sel:[0,0,1]
	global_store_dword v[122:123], v128, off
	ds_read_b128 v[124:127], v167
	ds_read_b128 v[128:131], v167 offset:32768
	s_waitcnt lgkmcnt(1)
	v_pk_fma_f32 v[194:195], v[124:125], v[190:191], 0 op_sel_hi:[1,0,0]
	v_pk_fma_f32 v[196:197], v[126:127], v[190:191], 0 op_sel_hi:[1,0,0]
	s_waitcnt lgkmcnt(0)
	v_pk_fma_f32 v[198:199], v[190:191], v[128:129], 0 op_sel_hi:[0,1,0]
	v_pk_fma_f32 v[200:201], v[190:191], v[130:131], 0 op_sel_hi:[0,1,0]
	v_pk_fma_f32 v[202:203], v[124:125], v[192:193], 0 op_sel_hi:[1,0,0]
	v_pk_fma_f32 v[204:205], v[126:127], v[192:193], 0 op_sel_hi:[1,0,0]
	v_pk_fma_f32 v[206:207], v[128:129], v[192:193], 0 op_sel_hi:[1,0,0]
	v_pk_fma_f32 v[208:209], v[130:131], v[192:193], 0 op_sel_hi:[1,0,0]
	ds_read_b128 v[124:127], v167 offset:1024
	ds_read_b128 v[128:131], v167 offset:33792
	s_waitcnt lgkmcnt(1)
	v_pk_fma_f32 v[196:197], v[190:191], v[126:127], v[196:197] op_sel:[1,0,0]
	v_pk_fma_f32 v[194:195], v[190:191], v[124:125], v[194:195] op_sel:[1,0,0]
	s_waitcnt lgkmcnt(0)
	v_pk_fma_f32 v[200:201], v[190:191], v[130:131], v[200:201] op_sel:[1,0,0]
	v_pk_fma_f32 v[190:191], v[190:191], v[128:129], v[198:199] op_sel:[1,0,0]
	v_pk_fma_f32 v[198:199], v[192:193], v[126:127], v[204:205] op_sel:[1,0,0]
	v_pk_fma_f32 v[202:203], v[192:193], v[124:125], v[202:203] op_sel:[1,0,0]
	v_pk_fma_f32 v[204:205], v[192:193], v[130:131], v[208:209] op_sel:[1,0,0]
	v_pk_fma_f32 v[192:193], v[192:193], v[128:129], v[206:207] op_sel:[1,0,0]
	ds_read_b128 v[124:127], v167 offset:2048
	ds_read_b128 v[128:131], v167 offset:34816
	s_waitcnt lgkmcnt(1)
	v_pk_fma_f32 v[194:195], v[188:189], v[124:125], v[194:195] op_sel_hi:[0,1,1]
	v_pk_fma_f32 v[196:197], v[188:189], v[126:127], v[196:197] op_sel_hi:[0,1,1]
	s_waitcnt lgkmcnt(0)
	v_pk_fma_f32 v[190:191], v[188:189], v[128:129], v[190:191] op_sel_hi:[0,1,1]
	v_pk_fma_f32 v[200:201], v[188:189], v[130:131], v[200:201] op_sel_hi:[0,1,1]
	v_pk_fma_f32 v[202:203], v[132:133], v[124:125], v[202:203] op_sel_hi:[0,1,1]
	v_pk_fma_f32 v[198:199], v[132:133], v[126:127], v[198:199] op_sel_hi:[0,1,1]
	v_pk_fma_f32 v[192:193], v[132:133], v[128:129], v[192:193] op_sel_hi:[0,1,1]
	v_pk_fma_f32 v[204:205], v[132:133], v[130:131], v[204:205] op_sel_hi:[0,1,1]
	ds_read_b128 v[124:127], v167 offset:3072
	ds_read_b128 v[128:131], v167 offset:35840
	s_waitcnt lgkmcnt(1)
	v_pk_fma_f32 v[196:197], v[188:189], v[126:127], v[196:197] op_sel:[1,0,0]
	v_pk_fma_f32 v[194:195], v[188:189], v[124:125], v[194:195] op_sel:[1,0,0]
	s_waitcnt lgkmcnt(0)
	v_pk_fma_f32 v[200:201], v[188:189], v[130:131], v[200:201] op_sel:[1,0,0]
	v_pk_fma_f32 v[188:189], v[188:189], v[128:129], v[190:191] op_sel:[1,0,0]
	v_pk_fma_f32 v[190:191], v[132:133], v[126:127], v[198:199] op_sel:[1,0,0]
	v_pk_fma_f32 v[198:199], v[132:133], v[124:125], v[202:203] op_sel:[1,0,0]
	global_load_dwordx4 v[124:127], v[142:143], off
	v_pk_fma_f32 v[128:129], v[132:133], v[128:129], v[192:193] op_sel:[1,0,0]
	v_pk_fma_f32 v[130:131], v[132:133], v[130:131], v[204:205] op_sel:[1,0,0]
	s_waitcnt vmcnt(0)
	v_pk_mul_f32 v[192:193], v[114:115], v[124:125]
	v_pk_mul_f32 v[114:115], v[118:119], v[138:139] op_sel_hi:[1,0]
	s_nop 0
	v_pk_mul_f32 v[124:125], v[114:115], v[124:125]
	v_med3_f32 v114, v192, s78, v179
	v_med3_f32 v115, v193, s78, v179
	v_cvt_pk_fp8_f32 v118, v114, v115
	v_pk_mul_f32 v[132:133], v[116:117], v[126:127]
	v_pk_mul_f32 v[116:117], v[120:121], v[138:139] op_sel_hi:[1,0]
	v_med3_f32 v114, v124, s78, v179
	v_pk_mul_f32 v[126:127], v[116:117], v[126:127]
	v_med3_f32 v116, v132, s78, v179
	v_med3_f32 v117, v133, s78, v179
	v_cvt_pk_fp8_f32 v118, v116, v117 op_sel:[0,0,1]
	v_med3_f32 v115, v125, s78, v179
	v_med3_f32 v116, v126, s78, v179
	v_med3_f32 v117, v127, s78, v179
	global_store_dword v[122:123], v118, off offset:-1792
	s_nop 0
	v_cvt_pk_fp8_f32 v118, v114, v115
	v_cvt_pk_fp8_f32 v118, v116, v117 op_sel:[0,0,1]
	global_store_dword v[122:123], v118, off offset:256
	ds_read_b128 v[114:117], v167 offset:4096
	ds_read_b128 v[118:121], v167 offset:36864
	s_waitcnt lgkmcnt(1)
	v_pk_fma_f32 v[194:195], v[192:193], v[114:115], v[194:195] op_sel_hi:[0,1,1]
	v_pk_fma_f32 v[196:197], v[192:193], v[116:117], v[196:197] op_sel_hi:[0,1,1]
	s_waitcnt lgkmcnt(0)
	v_pk_fma_f32 v[188:189], v[192:193], v[118:119], v[188:189] op_sel_hi:[0,1,1]
	v_pk_fma_f32 v[200:201], v[192:193], v[120:121], v[200:201] op_sel_hi:[0,1,1]
	v_pk_fma_f32 v[198:199], v[124:125], v[114:115], v[198:199] op_sel_hi:[0,1,1]
	v_pk_fma_f32 v[190:191], v[124:125], v[116:117], v[190:191] op_sel_hi:[0,1,1]
	v_pk_fma_f32 v[128:129], v[124:125], v[118:119], v[128:129] op_sel_hi:[0,1,1]
	v_pk_fma_f32 v[130:131], v[124:125], v[120:121], v[130:131] op_sel_hi:[0,1,1]
	ds_read_b128 v[114:117], v167 offset:5120
	ds_read_b128 v[118:121], v167 offset:37888
	s_waitcnt lgkmcnt(1)
	v_pk_fma_f32 v[196:197], v[192:193], v[116:117], v[196:197] op_sel:[1,0,0]
	v_pk_fma_f32 v[194:195], v[192:193], v[114:115], v[194:195] op_sel:[1,0,0]
	s_waitcnt lgkmcnt(0)
	v_pk_fma_f32 v[200:201], v[192:193], v[120:121], v[200:201] op_sel:[1,0,0]
	v_pk_fma_f32 v[188:189], v[192:193], v[118:119], v[188:189] op_sel:[1,0,0]
	v_pk_fma_f32 v[190:191], v[124:125], v[116:117], v[190:191] op_sel:[1,0,0]
	v_pk_fma_f32 v[192:193], v[124:125], v[114:115], v[198:199] op_sel:[1,0,0]
	v_pk_fma_f32 v[130:131], v[124:125], v[120:121], v[130:131] op_sel:[1,0,0]
	v_pk_fma_f32 v[124:125], v[124:125], v[118:119], v[128:129] op_sel:[1,0,0]
	ds_read_b128 v[114:117], v167 offset:6144
	ds_read_b128 v[118:121], v167 offset:38912
	s_waitcnt lgkmcnt(1)
	v_pk_fma_f32 v[128:129], v[132:133], v[114:115], v[194:195] op_sel_hi:[0,1,1]
	v_pk_fma_f32 v[194:195], v[132:133], v[116:117], v[196:197] op_sel_hi:[0,1,1]
	s_waitcnt lgkmcnt(0)
	v_pk_fma_f32 v[188:189], v[132:133], v[118:119], v[188:189] op_sel_hi:[0,1,1]
	v_pk_fma_f32 v[196:197], v[132:133], v[120:121], v[200:201] op_sel_hi:[0,1,1]
	v_pk_fma_f32 v[192:193], v[126:127], v[114:115], v[192:193] op_sel_hi:[0,1,1]
	v_pk_fma_f32 v[190:191], v[126:127], v[116:117], v[190:191] op_sel_hi:[0,1,1]
	v_pk_fma_f32 v[124:125], v[126:127], v[118:119], v[124:125] op_sel_hi:[0,1,1]
	v_pk_fma_f32 v[130:131], v[126:127], v[120:121], v[130:131] op_sel_hi:[0,1,1]
	ds_read_b128 v[114:117], v167 offset:7168
	ds_read_b128 v[118:121], v167 offset:39936
	s_waitcnt lgkmcnt(1)
	v_pk_fma_f32 v[194:195], v[132:133], v[116:117], v[194:195] op_sel:[1,0,0]
	v_pk_fma_f32 v[128:129], v[132:133], v[114:115], v[128:129] op_sel:[1,0,0]
	s_waitcnt lgkmcnt(0)
	v_pk_fma_f32 v[196:197], v[132:133], v[120:121], v[196:197] op_sel:[1,0,0]
	v_pk_fma_f32 v[132:133], v[132:133], v[118:119], v[188:189] op_sel:[1,0,0]
	v_pk_fma_f32 v[188:189], v[126:127], v[116:117], v[190:191] op_sel:[1,0,0]
	v_pk_fma_f32 v[190:191], v[126:127], v[114:115], v[192:193] op_sel:[1,0,0]
	global_load_dwordx4 v[114:117], v[144:145], off
	v_pk_fma_f32 v[118:119], v[126:127], v[118:119], v[124:125] op_sel:[1,0,0]
	v_pk_fma_f32 v[120:121], v[126:127], v[120:121], v[130:131] op_sel:[1,0,0]
	s_waitcnt vmcnt(0)
	v_pk_mul_f32 v[124:125], v[106:107], v[114:115]
	v_pk_mul_f32 v[106:107], v[110:111], v[138:139] op_sel_hi:[1,0]
	s_nop 0
	v_pk_mul_f32 v[114:115], v[106:107], v[114:115]
	v_med3_f32 v106, v124, s78, v179
	v_med3_f32 v107, v125, s78, v179
	v_cvt_pk_fp8_f32 v110, v106, v107
	v_pk_mul_f32 v[130:131], v[108:109], v[116:117]
	v_pk_mul_f32 v[108:109], v[112:113], v[138:139] op_sel_hi:[1,0]
	v_med3_f32 v106, v114, s78, v179
	v_pk_mul_f32 v[192:193], v[108:109], v[116:117]
	v_med3_f32 v108, v130, s78, v179
	v_med3_f32 v109, v131, s78, v179
	v_cvt_pk_fp8_f32 v110, v108, v109 op_sel:[0,0,1]
	v_med3_f32 v107, v115, s78, v179
	v_med3_f32 v108, v192, s78, v179
	v_med3_f32 v109, v193, s78, v179
	global_store_dword v[122:123], v110, off offset:-1536
	s_nop 0
	v_cvt_pk_fp8_f32 v110, v106, v107
	v_cvt_pk_fp8_f32 v110, v108, v109 op_sel:[0,0,1]
	global_store_dword v[122:123], v110, off offset:512
	ds_read_b128 v[106:109], v167 offset:8192
	ds_read_b128 v[110:113], v167 offset:40960
	s_waitcnt lgkmcnt(1)
	v_pk_fma_f32 v[116:117], v[124:125], v[106:107], v[128:129] op_sel_hi:[0,1,1]
	v_pk_fma_f32 v[126:127], v[124:125], v[108:109], v[194:195] op_sel_hi:[0,1,1]
	s_waitcnt lgkmcnt(0)
	v_pk_fma_f32 v[128:129], v[124:125], v[110:111], v[132:133] op_sel_hi:[0,1,1]
	v_pk_fma_f32 v[132:133], v[124:125], v[112:113], v[196:197] op_sel_hi:[0,1,1]
	v_pk_fma_f32 v[190:191], v[114:115], v[106:107], v[190:191] op_sel_hi:[0,1,1]
	v_pk_fma_f32 v[188:189], v[114:115], v[108:109], v[188:189] op_sel_hi:[0,1,1]
	v_pk_fma_f32 v[118:119], v[114:115], v[110:111], v[118:119] op_sel_hi:[0,1,1]
	v_pk_fma_f32 v[120:121], v[114:115], v[112:113], v[120:121] op_sel_hi:[0,1,1]
	ds_read_b128 v[106:109], v167 offset:9216
	ds_read_b128 v[110:113], v167 offset:41984
	s_waitcnt lgkmcnt(1)
	v_pk_fma_f32 v[126:127], v[124:125], v[108:109], v[126:127] op_sel:[1,0,0]
	v_pk_fma_f32 v[116:117], v[124:125], v[106:107], v[116:117] op_sel:[1,0,0]
	s_waitcnt lgkmcnt(0)
	v_pk_fma_f32 v[132:133], v[124:125], v[112:113], v[132:133] op_sel:[1,0,0]
	v_pk_fma_f32 v[124:125], v[124:125], v[110:111], v[128:129] op_sel:[1,0,0]
	v_pk_fma_f32 v[128:129], v[114:115], v[108:109], v[188:189] op_sel:[1,0,0]
	v_pk_fma_f32 v[188:189], v[114:115], v[106:107], v[190:191] op_sel:[1,0,0]
	v_pk_fma_f32 v[120:121], v[114:115], v[112:113], v[120:121] op_sel:[1,0,0]
	v_pk_fma_f32 v[114:115], v[114:115], v[110:111], v[118:119] op_sel:[1,0,0]
	ds_read_b128 v[106:109], v167 offset:10240
	ds_read_b128 v[110:113], v167 offset:43008
	s_waitcnt lgkmcnt(1)
	v_pk_fma_f32 v[190:191], v[130:131], v[108:109], v[126:127] op_sel_hi:[0,1,1]
	s_waitcnt lgkmcnt(0)
	v_pk_fma_f32 v[194:195], v[130:131], v[110:111], v[124:125] op_sel_hi:[0,1,1]
	v_pk_fma_f32 v[132:133], v[130:131], v[112:113], v[132:133] op_sel_hi:[0,1,1]
	v_pk_fma_f32 v[112:113], v[192:193], v[112:113], v[120:121] op_sel_hi:[0,1,1]
	ds_read_b128 v[118:121], v167 offset:11264
	ds_read_b128 v[124:127], v167 offset:44032
	v_pk_fma_f32 v[116:117], v[130:131], v[106:107], v[116:117] op_sel_hi:[0,1,1]
	v_pk_fma_f32 v[128:129], v[192:193], v[108:109], v[128:129] op_sel_hi:[0,1,1]
	v_pk_fma_f32 v[196:197], v[192:193], v[110:111], v[114:115] op_sel_hi:[0,1,1]
	v_pk_fma_f32 v[188:189], v[192:193], v[106:107], v[188:189] op_sel_hi:[0,1,1]
	s_waitcnt lgkmcnt(1)
	v_pk_fma_f32 v[106:107], v[130:131], v[120:121], v[190:191] op_sel:[1,0,0]
	v_pk_fma_f32 v[114:115], v[130:131], v[118:119], v[116:117] op_sel:[1,0,0]
	s_waitcnt lgkmcnt(0)
	v_pk_fma_f32 v[108:109], v[130:131], v[126:127], v[132:133] op_sel:[1,0,0]
	v_pk_fma_f32 v[116:117], v[130:131], v[124:125], v[194:195] op_sel:[1,0,0]
	v_pk_fma_f32 v[110:111], v[192:193], v[120:121], v[128:129] op_sel:[1,0,0]
	v_pk_fma_f32 v[112:113], v[192:193], v[126:127], v[112:113] op_sel:[1,0,0]
	v_pk_fma_f32 v[120:121], v[192:193], v[124:125], v[196:197] op_sel:[1,0,0]
	global_load_dwordx4 v[124:127], v[148:149], off
	v_pk_fma_f32 v[118:119], v[192:193], v[118:119], v[188:189] op_sel:[1,0,0]
	s_waitcnt vmcnt(0)
	v_pk_mul_f32 v[130:131], v[98:99], v[124:125]
	v_pk_mul_f32 v[98:99], v[102:103], v[138:139] op_sel_hi:[1,0]
	s_nop 0
	v_pk_mul_f32 v[124:125], v[98:99], v[124:125]
	v_med3_f32 v98, v130, s78, v179
	v_med3_f32 v99, v131, s78, v179
	v_cvt_pk_fp8_f32 v102, v98, v99
	v_pk_mul_f32 v[128:129], v[100:101], v[126:127]
	v_pk_mul_f32 v[100:101], v[104:105], v[138:139] op_sel_hi:[1,0]
	v_med3_f32 v98, v124, s78, v179
	v_pk_mul_f32 v[126:127], v[100:101], v[126:127]
	v_med3_f32 v100, v128, s78, v179
	v_med3_f32 v101, v129, s78, v179
	v_cvt_pk_fp8_f32 v102, v100, v101 op_sel:[0,0,1]
	v_med3_f32 v99, v125, s78, v179
	v_med3_f32 v100, v126, s78, v179
	v_med3_f32 v101, v127, s78, v179
	global_store_dword v[122:123], v102, off offset:-1280
	s_nop 0
	v_cvt_pk_fp8_f32 v102, v98, v99
	v_cvt_pk_fp8_f32 v102, v100, v101 op_sel:[0,0,1]
	global_store_dword v[122:123], v102, off offset:768
	ds_read_b128 v[98:101], v167 offset:12288
	ds_read_b128 v[102:105], v167 offset:45056
	s_waitcnt lgkmcnt(1)
	v_pk_fma_f32 v[114:115], v[130:131], v[98:99], v[114:115] op_sel_hi:[0,1,1]
	v_pk_fma_f32 v[106:107], v[130:131], v[100:101], v[106:107] op_sel_hi:[0,1,1]
	s_waitcnt lgkmcnt(0)
	v_pk_fma_f32 v[116:117], v[130:131], v[102:103], v[116:117] op_sel_hi:[0,1,1]
	v_pk_fma_f32 v[108:109], v[130:131], v[104:105], v[108:109] op_sel_hi:[0,1,1]
	v_pk_fma_f32 v[118:119], v[124:125], v[98:99], v[118:119] op_sel_hi:[0,1,1]
	v_pk_fma_f32 v[110:111], v[124:125], v[100:101], v[110:111] op_sel_hi:[0,1,1]
	v_pk_fma_f32 v[120:121], v[124:125], v[102:103], v[120:121] op_sel_hi:[0,1,1]
	v_pk_fma_f32 v[112:113], v[124:125], v[104:105], v[112:113] op_sel_hi:[0,1,1]
	ds_read_b128 v[98:101], v167 offset:13312
	ds_read_b128 v[102:105], v167 offset:46080
	s_waitcnt lgkmcnt(1)
	v_pk_fma_f32 v[106:107], v[130:131], v[100:101], v[106:107] op_sel:[1,0,0]
	v_pk_fma_f32 v[114:115], v[130:131], v[98:99], v[114:115] op_sel:[1,0,0]
	s_waitcnt lgkmcnt(0)
	v_pk_fma_f32 v[108:109], v[130:131], v[104:105], v[108:109] op_sel:[1,0,0]
	v_pk_fma_f32 v[116:117], v[130:131], v[102:103], v[116:117] op_sel:[1,0,0]
	v_pk_fma_f32 v[110:111], v[124:125], v[100:101], v[110:111] op_sel:[1,0,0]
	v_pk_fma_f32 v[118:119], v[124:125], v[98:99], v[118:119] op_sel:[1,0,0]
	v_pk_fma_f32 v[112:113], v[124:125], v[104:105], v[112:113] op_sel:[1,0,0]
	v_pk_fma_f32 v[120:121], v[124:125], v[102:103], v[120:121] op_sel:[1,0,0]
	ds_read_b128 v[98:101], v167 offset:14336
	ds_read_b128 v[102:105], v167 offset:47104
	s_waitcnt lgkmcnt(1)
	v_pk_fma_f32 v[124:125], v[128:129], v[98:99], v[114:115] op_sel_hi:[0,1,1]
	s_waitcnt lgkmcnt(0)
	v_pk_fma_f32 v[130:131], v[128:129], v[102:103], v[116:117] op_sel_hi:[0,1,1]
	v_pk_fma_f32 v[108:109], v[128:129], v[104:105], v[108:109] op_sel_hi:[0,1,1]
	v_pk_fma_f32 v[132:133], v[126:127], v[100:101], v[110:111] op_sel_hi:[0,1,1]
	v_pk_fma_f32 v[104:105], v[126:127], v[104:105], v[112:113] op_sel_hi:[0,1,1]
	ds_read_b128 v[110:113], v167 offset:15360
	ds_read_b128 v[114:117], v167 offset:48128
	v_pk_fma_f32 v[106:107], v[128:129], v[100:101], v[106:107] op_sel_hi:[0,1,1]
	v_pk_fma_f32 v[118:119], v[126:127], v[98:99], v[118:119] op_sel_hi:[0,1,1]
	v_pk_fma_f32 v[120:121], v[126:127], v[102:103], v[120:121] op_sel_hi:[0,1,1]
	s_waitcnt lgkmcnt(1)
	v_pk_fma_f32 v[98:99], v[128:129], v[112:113], v[106:107] op_sel:[1,0,0]
	v_pk_fma_f32 v[106:107], v[128:129], v[110:111], v[124:125] op_sel:[1,0,0]
	s_waitcnt lgkmcnt(0)
	v_pk_fma_f32 v[100:101], v[128:129], v[116:117], v[108:109] op_sel:[1,0,0]
	v_pk_fma_f32 v[110:111], v[126:127], v[110:111], v[118:119] op_sel:[1,0,0]
	v_pk_fma_f32 v[104:105], v[126:127], v[116:117], v[104:105] op_sel:[1,0,0]
	global_load_dwordx4 v[116:119], v[150:151], off
	v_pk_fma_f32 v[108:109], v[128:129], v[114:115], v[130:131] op_sel:[1,0,0]
	v_pk_fma_f32 v[102:103], v[126:127], v[112:113], v[132:133] op_sel:[1,0,0]
	v_pk_fma_f32 v[112:113], v[126:127], v[114:115], v[120:121] op_sel:[1,0,0]
	v_pk_mul_f32 v[114:115], v[94:95], v[162:163] op_sel_hi:[1,0]
	v_pk_mul_f32 v[94:95], v[96:97], v[162:163] op_sel_hi:[1,0]
	s_waitcnt vmcnt(0)
	v_pk_mul_f32 v[96:97], v[114:115], v[116:117]
	v_pk_mul_f32 v[94:95], v[94:95], v[118:119]
	v_pk_mul_f32 v[114:115], v[92:93], v[118:119]
	v_med3_f32 v92, v96, s78, v179
	v_med3_f32 v93, v97, s78, v179
	s_nop 0
	v_cvt_pk_fp8_f32 v118, v92, v93
	v_pk_mul_f32 v[90:91], v[90:91], v[116:117]
	v_med3_f32 v116, v94, s78, v179
	v_med3_f32 v117, v95, s78, v179
	v_cvt_pk_fp8_f32 v118, v116, v117 op_sel:[0,0,1]
	v_med3_f32 v92, v90, s78, v179
	v_med3_f32 v93, v91, s78, v179
	v_med3_f32 v116, v114, s78, v179
	global_store_dword v[122:123], v118, off offset:-1024
	s_nop 0
	v_cvt_pk_fp8_f32 v118, v92, v93
	v_med3_f32 v117, v115, s78, v179
	v_cvt_pk_fp8_f32 v118, v116, v117 op_sel:[0,0,1]
	global_store_dword v[122:123], v118, off offset:1024
	ds_read_b128 v[116:119], v167 offset:16384
	ds_read_b128 v[124:127], v167 offset:49152
	s_waitcnt lgkmcnt(1)
	v_pk_fma_f32 v[92:93], v[96:97], v[116:117], v[106:107] op_sel_hi:[0,1,1]
	v_pk_fma_f32 v[106:107], v[96:97], v[118:119], v[98:99] op_sel_hi:[0,1,1]
	s_waitcnt lgkmcnt(0)
	v_pk_fma_f32 v[120:121], v[96:97], v[126:127], v[100:101] op_sel_hi:[0,1,1]
	v_pk_fma_f32 v[110:111], v[90:91], v[116:117], v[110:111] op_sel_hi:[0,1,1]
	v_pk_fma_f32 v[116:117], v[90:91], v[118:119], v[102:103] op_sel_hi:[0,1,1]
	v_pk_fma_f32 v[118:119], v[90:91], v[126:127], v[104:105] op_sel_hi:[0,1,1]
	ds_read_b128 v[98:101], v167 offset:17408
	ds_read_b128 v[102:105], v167 offset:50176
	v_pk_fma_f32 v[108:109], v[96:97], v[124:125], v[108:109] op_sel_hi:[0,1,1]
	v_pk_fma_f32 v[112:113], v[90:91], v[124:125], v[112:113] op_sel_hi:[0,1,1]
	s_waitcnt lgkmcnt(1)
	v_pk_fma_f32 v[106:107], v[96:97], v[100:101], v[106:107] op_sel:[1,0,0]
	v_pk_fma_f32 v[124:125], v[96:97], v[98:99], v[92:93] op_sel:[1,0,0]
	s_waitcnt lgkmcnt(0)
	v_pk_fma_f32 v[120:121], v[96:97], v[104:105], v[120:121] op_sel:[1,0,0]
	v_pk_fma_f32 v[108:109], v[96:97], v[102:103], v[108:109] op_sel:[1,0,0]
	v_pk_fma_f32 v[100:101], v[90:91], v[100:101], v[116:117] op_sel:[1,0,0]
	v_pk_fma_f32 v[110:111], v[90:91], v[98:99], v[110:111] op_sel:[1,0,0]
	v_pk_fma_f32 v[104:105], v[90:91], v[104:105], v[118:119] op_sel:[1,0,0]
	v_pk_fma_f32 v[102:103], v[90:91], v[102:103], v[112:113] op_sel:[1,0,0]
	ds_read_b128 v[90:93], v167 offset:18432
	ds_read_b128 v[96:99], v167 offset:51200
	s_waitcnt lgkmcnt(1)
	v_pk_fma_f32 v[116:117], v[94:95], v[92:93], v[106:107] op_sel_hi:[0,1,1]
	s_waitcnt lgkmcnt(0)
	v_pk_fma_f32 v[118:119], v[94:95], v[96:97], v[108:109] op_sel_hi:[0,1,1]
	v_pk_fma_f32 v[126:127], v[114:115], v[96:97], v[102:103] op_sel_hi:[0,1,1]
	v_pk_fma_f32 v[96:97], v[114:115], v[98:99], v[104:105] op_sel_hi:[0,1,1]
	ds_read_b128 v[102:105], v167 offset:19456
	ds_read_b128 v[106:109], v167 offset:52224
	v_pk_fma_f32 v[112:113], v[94:95], v[90:91], v[124:125] op_sel_hi:[0,1,1]
	v_pk_fma_f32 v[120:121], v[94:95], v[98:99], v[120:121] op_sel_hi:[0,1,1]
	v_pk_fma_f32 v[124:125], v[114:115], v[92:93], v[100:101] op_sel_hi:[0,1,1]
	v_pk_fma_f32 v[110:111], v[114:115], v[90:91], v[110:111] op_sel_hi:[0,1,1]
	s_waitcnt lgkmcnt(1)
	v_pk_fma_f32 v[90:91], v[94:95], v[104:105], v[116:117] op_sel:[1,0,0]
	v_pk_fma_f32 v[98:99], v[94:95], v[102:103], v[112:113] op_sel:[1,0,0]
	s_waitcnt lgkmcnt(0)
	v_pk_fma_f32 v[92:93], v[94:95], v[108:109], v[120:121] op_sel:[1,0,0]
	v_pk_fma_f32 v[100:101], v[94:95], v[106:107], v[118:119] op_sel:[1,0,0]
	v_pk_fma_f32 v[94:95], v[114:115], v[104:105], v[124:125] op_sel:[1,0,0]
	v_pk_fma_f32 v[96:97], v[114:115], v[108:109], v[96:97] op_sel:[1,0,0]
	v_pk_fma_f32 v[104:105], v[114:115], v[106:107], v[126:127] op_sel:[1,0,0]
	global_load_dwordx4 v[106:109], v[152:153], off
	v_pk_fma_f32 v[102:103], v[114:115], v[102:103], v[110:111] op_sel:[1,0,0]
	s_waitcnt vmcnt(0)
	v_pk_mul_f32 v[112:113], v[82:83], v[106:107]
	v_pk_mul_f32 v[82:83], v[86:87], v[138:139] op_sel_hi:[1,0]
	s_nop 0
	v_pk_mul_f32 v[106:107], v[82:83], v[106:107]
	v_med3_f32 v82, v112, s78, v179
	v_med3_f32 v83, v113, s78, v179
	v_cvt_pk_fp8_f32 v86, v82, v83
	v_pk_mul_f32 v[110:111], v[84:85], v[108:109]
	v_pk_mul_f32 v[84:85], v[88:89], v[138:139] op_sel_hi:[1,0]
	v_med3_f32 v82, v106, s78, v179
	v_pk_mul_f32 v[108:109], v[84:85], v[108:109]
	v_med3_f32 v84, v110, s78, v179
	v_med3_f32 v85, v111, s78, v179
	v_cvt_pk_fp8_f32 v86, v84, v85 op_sel:[0,0,1]
	v_med3_f32 v83, v107, s78, v179
	v_med3_f32 v84, v108, s78, v179
	v_med3_f32 v85, v109, s78, v179
	global_store_dword v[122:123], v86, off offset:-768
	s_nop 0
	v_cvt_pk_fp8_f32 v86, v82, v83
	v_cvt_pk_fp8_f32 v86, v84, v85 op_sel:[0,0,1]
	global_store_dword v[122:123], v86, off offset:1280
	ds_read_b128 v[82:85], v167 offset:20480
	ds_read_b128 v[86:89], v167 offset:53248
	s_waitcnt lgkmcnt(1)
	v_pk_fma_f32 v[98:99], v[112:113], v[82:83], v[98:99] op_sel_hi:[0,1,1]
	v_pk_fma_f32 v[90:91], v[112:113], v[84:85], v[90:91] op_sel_hi:[0,1,1]
	s_waitcnt lgkmcnt(0)
	v_pk_fma_f32 v[100:101], v[112:113], v[86:87], v[100:101] op_sel_hi:[0,1,1]
	v_pk_fma_f32 v[92:93], v[112:113], v[88:89], v[92:93] op_sel_hi:[0,1,1]
	v_pk_fma_f32 v[102:103], v[106:107], v[82:83], v[102:103] op_sel_hi:[0,1,1]
	v_pk_fma_f32 v[94:95], v[106:107], v[84:85], v[94:95] op_sel_hi:[0,1,1]
	v_pk_fma_f32 v[104:105], v[106:107], v[86:87], v[104:105] op_sel_hi:[0,1,1]
	v_pk_fma_f32 v[96:97], v[106:107], v[88:89], v[96:97] op_sel_hi:[0,1,1]
	ds_read_b128 v[82:85], v167 offset:21504
	ds_read_b128 v[86:89], v167 offset:54272
	s_waitcnt lgkmcnt(1)
	v_pk_fma_f32 v[90:91], v[112:113], v[84:85], v[90:91] op_sel:[1,0,0]
	v_pk_fma_f32 v[98:99], v[112:113], v[82:83], v[98:99] op_sel:[1,0,0]
	s_waitcnt lgkmcnt(0)
	v_pk_fma_f32 v[92:93], v[112:113], v[88:89], v[92:93] op_sel:[1,0,0]
	v_pk_fma_f32 v[100:101], v[112:113], v[86:87], v[100:101] op_sel:[1,0,0]
	v_pk_fma_f32 v[94:95], v[106:107], v[84:85], v[94:95] op_sel:[1,0,0]
	v_pk_fma_f32 v[102:103], v[106:107], v[82:83], v[102:103] op_sel:[1,0,0]
	v_pk_fma_f32 v[96:97], v[106:107], v[88:89], v[96:97] op_sel:[1,0,0]
	v_pk_fma_f32 v[104:105], v[106:107], v[86:87], v[104:105] op_sel:[1,0,0]
	ds_read_b128 v[82:85], v167 offset:22528
	ds_read_b128 v[86:89], v167 offset:55296
	s_waitcnt lgkmcnt(1)
	v_pk_fma_f32 v[98:99], v[110:111], v[82:83], v[98:99] op_sel_hi:[0,1,1]
	v_pk_fma_f32 v[90:91], v[110:111], v[84:85], v[90:91] op_sel_hi:[0,1,1]
	s_waitcnt lgkmcnt(0)
	v_pk_fma_f32 v[106:107], v[110:111], v[86:87], v[100:101] op_sel_hi:[0,1,1]
	v_pk_fma_f32 v[112:113], v[108:109], v[82:83], v[102:103] op_sel_hi:[0,1,1]
	v_pk_fma_f32 v[114:115], v[108:109], v[84:85], v[94:95] op_sel_hi:[0,1,1]
	ds_read_b128 v[82:85], v167 offset:23552
	ds_read_b128 v[100:103], v167 offset:56320
	v_pk_fma_f32 v[104:105], v[108:109], v[86:87], v[104:105] op_sel_hi:[0,1,1]
	v_pk_fma_f32 v[116:117], v[108:109], v[88:89], v[96:97] op_sel_hi:[0,1,1]
	v_pk_fma_f32 v[92:93], v[110:111], v[88:89], v[92:93] op_sel_hi:[0,1,1]
	s_waitcnt lgkmcnt(1)
	v_pk_fma_f32 v[86:87], v[110:111], v[84:85], v[90:91] op_sel:[1,0,0]
	v_pk_fma_f32 v[94:95], v[110:111], v[82:83], v[98:99] op_sel:[1,0,0]
	v_pk_fma_f32 v[90:91], v[108:109], v[84:85], v[114:115] op_sel:[1,0,0]
	v_pk_fma_f32 v[98:99], v[108:109], v[82:83], v[112:113] op_sel:[1,0,0]
	global_load_dwordx4 v[82:85], v[154:155], off
	s_waitcnt lgkmcnt(0)
	v_pk_fma_f32 v[96:97], v[110:111], v[100:101], v[106:107] op_sel:[1,0,0]
	v_pk_fma_f32 v[100:101], v[108:109], v[100:101], v[104:105] op_sel:[1,0,0]
	v_pk_fma_f32 v[88:89], v[110:111], v[102:103], v[92:93] op_sel:[1,0,0]
	v_pk_fma_f32 v[92:93], v[108:109], v[102:103], v[116:117] op_sel:[1,0,0]
	s_waitcnt vmcnt(0)
	v_pk_mul_f32 v[104:105], v[74:75], v[82:83]
	v_pk_mul_f32 v[74:75], v[78:79], v[138:139] op_sel_hi:[1,0]
	s_nop 0
	v_pk_mul_f32 v[82:83], v[74:75], v[82:83]
	v_med3_f32 v74, v104, s78, v179
	v_med3_f32 v75, v105, s78, v179
	v_cvt_pk_fp8_f32 v78, v74, v75
	v_pk_mul_f32 v[102:103], v[76:77], v[84:85]
	v_pk_mul_f32 v[76:77], v[80:81], v[138:139] op_sel_hi:[1,0]
	v_med3_f32 v74, v82, s78, v179
	v_pk_mul_f32 v[106:107], v[76:77], v[84:85]
	v_med3_f32 v76, v102, s78, v179
	v_med3_f32 v77, v103, s78, v179
	v_cvt_pk_fp8_f32 v78, v76, v77 op_sel:[0,0,1]
	v_med3_f32 v75, v83, s78, v179
	v_med3_f32 v76, v106, s78, v179
	v_med3_f32 v77, v107, s78, v179
	global_store_dword v[122:123], v78, off offset:-512
	s_nop 0
	v_cvt_pk_fp8_f32 v78, v74, v75
	v_cvt_pk_fp8_f32 v78, v76, v77 op_sel:[0,0,1]
	global_store_dword v[122:123], v78, off offset:1536
	ds_read_b128 v[74:77], v167 offset:24576
	ds_read_b128 v[78:81], v167 offset:57344
	s_waitcnt lgkmcnt(1)
	v_pk_fma_f32 v[84:85], v[104:105], v[74:75], v[94:95] op_sel_hi:[0,1,1]
	v_pk_fma_f32 v[86:87], v[104:105], v[76:77], v[86:87] op_sel_hi:[0,1,1]
	s_waitcnt lgkmcnt(0)
	v_pk_fma_f32 v[94:95], v[104:105], v[78:79], v[96:97] op_sel_hi:[0,1,1]
	v_pk_fma_f32 v[88:89], v[104:105], v[80:81], v[88:89] op_sel_hi:[0,1,1]
	v_pk_fma_f32 v[96:97], v[82:83], v[74:75], v[98:99] op_sel_hi:[0,1,1]
	v_pk_fma_f32 v[90:91], v[82:83], v[76:77], v[90:91] op_sel_hi:[0,1,1]
	v_pk_fma_f32 v[98:99], v[82:83], v[78:79], v[100:101] op_sel_hi:[0,1,1]
	v_pk_fma_f32 v[92:93], v[82:83], v[80:81], v[92:93] op_sel_hi:[0,1,1]
	ds_read_b128 v[74:77], v167 offset:25600
	ds_read_b128 v[78:81], v167 offset:58368
	s_waitcnt lgkmcnt(1)
	v_pk_fma_f32 v[86:87], v[104:105], v[76:77], v[86:87] op_sel:[1,0,0]
	v_pk_fma_f32 v[84:85], v[104:105], v[74:75], v[84:85] op_sel:[1,0,0]
	s_waitcnt lgkmcnt(0)
	v_pk_fma_f32 v[88:89], v[104:105], v[80:81], v[88:89] op_sel:[1,0,0]
	v_pk_fma_f32 v[94:95], v[104:105], v[78:79], v[94:95] op_sel:[1,0,0]
	v_pk_fma_f32 v[90:91], v[82:83], v[76:77], v[90:91] op_sel:[1,0,0]
	v_pk_fma_f32 v[96:97], v[82:83], v[74:75], v[96:97] op_sel:[1,0,0]
	v_pk_fma_f32 v[92:93], v[82:83], v[80:81], v[92:93] op_sel:[1,0,0]
	v_pk_fma_f32 v[82:83], v[82:83], v[78:79], v[98:99] op_sel:[1,0,0]
	ds_read_b128 v[74:77], v167 offset:26624
	ds_read_b128 v[78:81], v167 offset:59392
	s_waitcnt lgkmcnt(1)
	v_pk_fma_f32 v[84:85], v[102:103], v[74:75], v[84:85] op_sel_hi:[0,1,1]
	v_pk_fma_f32 v[86:87], v[102:103], v[76:77], v[86:87] op_sel_hi:[0,1,1]
	s_waitcnt lgkmcnt(0)
	v_pk_fma_f32 v[94:95], v[102:103], v[78:79], v[94:95] op_sel_hi:[0,1,1]
	v_pk_fma_f32 v[88:89], v[102:103], v[80:81], v[88:89] op_sel_hi:[0,1,1]
	v_pk_fma_f32 v[96:97], v[106:107], v[74:75], v[96:97] op_sel_hi:[0,1,1]
	v_pk_fma_f32 v[98:99], v[106:107], v[76:77], v[90:91] op_sel_hi:[0,1,1]
	v_pk_fma_f32 v[100:101], v[106:107], v[78:79], v[82:83] op_sel_hi:[0,1,1]
	v_pk_fma_f32 v[104:105], v[106:107], v[80:81], v[92:93] op_sel_hi:[0,1,1]
	ds_read_b128 v[74:77], v167 offset:27648
	ds_read_b128 v[78:81], v167 offset:60416
	s_waitcnt lgkmcnt(1)
	v_pk_fma_f32 v[82:83], v[102:103], v[76:77], v[86:87] op_sel:[1,0,0]
	v_pk_fma_f32 v[90:91], v[102:103], v[74:75], v[84:85] op_sel:[1,0,0]
	s_waitcnt lgkmcnt(0)
	v_pk_fma_f32 v[92:93], v[102:103], v[78:79], v[94:95] op_sel:[1,0,0]
	v_pk_fma_f32 v[86:87], v[106:107], v[76:77], v[98:99] op_sel:[1,0,0]
	v_pk_fma_f32 v[94:95], v[106:107], v[74:75], v[96:97] op_sel:[1,0,0]
	global_load_dwordx4 v[74:77], v[156:157], off
	v_pk_fma_f32 v[84:85], v[102:103], v[80:81], v[88:89] op_sel:[1,0,0]
	v_pk_fma_f32 v[88:89], v[106:107], v[80:81], v[104:105] op_sel:[1,0,0]
	v_pk_fma_f32 v[96:97], v[106:107], v[78:79], v[100:101] op_sel:[1,0,0]
	s_waitcnt vmcnt(0)
	v_pk_mul_f32 v[80:81], v[70:71], v[74:75]
	v_pk_mul_f32 v[74:75], v[66:67], v[74:75]
	v_med3_f32 v66, v80, s78, v179
	v_med3_f32 v67, v81, s78, v179
	s_nop 0
	v_cvt_pk_fp8_f32 v70, v66, v67
	v_pk_mul_f32 v[78:79], v[72:73], v[76:77]
	v_pk_mul_f32 v[76:77], v[68:69], v[76:77]
	v_med3_f32 v68, v78, s78, v179
	v_med3_f32 v69, v79, s78, v179
	v_cvt_pk_fp8_f32 v70, v68, v69 op_sel:[0,0,1]
	v_med3_f32 v66, v74, s78, v179
	v_med3_f32 v67, v75, s78, v179
	v_med3_f32 v68, v76, s78, v179
	global_store_dword v[122:123], v70, off offset:-256
	s_nop 0
	v_cvt_pk_fp8_f32 v70, v66, v67
	v_med3_f32 v69, v77, s78, v179
	v_cvt_pk_fp8_f32 v70, v68, v69 op_sel:[0,0,1]
	global_store_dword v[122:123], v70, off offset:1792
	ds_read_b128 v[66:69], v167 offset:28672
	ds_read_b128 v[70:73], v167 offset:61440
	s_waitcnt lgkmcnt(1)
	v_pk_fma_f32 v[90:91], v[80:81], v[66:67], v[90:91] op_sel_hi:[0,1,1]
	v_pk_fma_f32 v[98:99], v[80:81], v[68:69], v[82:83] op_sel_hi:[0,1,1]
	s_waitcnt lgkmcnt(0)
	v_pk_fma_f32 v[82:83], v[80:81], v[70:71], v[92:93] op_sel_hi:[0,1,1]
	v_pk_fma_f32 v[92:93], v[80:81], v[72:73], v[84:85] op_sel_hi:[0,1,1]
	v_pk_fma_f32 v[84:85], v[74:75], v[66:67], v[94:95] op_sel_hi:[0,1,1]
	v_pk_fma_f32 v[94:95], v[74:75], v[68:69], v[86:87] op_sel_hi:[0,1,1]
	v_pk_fma_f32 v[86:87], v[74:75], v[70:71], v[96:97] op_sel_hi:[0,1,1]
	v_pk_fma_f32 v[88:89], v[74:75], v[72:73], v[88:89] op_sel_hi:[0,1,1]
	ds_read_b128 v[66:69], v167 offset:29696
	ds_read_b128 v[70:73], v167 offset:62464
	s_waitcnt lgkmcnt(1)
	v_pk_fma_f32 v[96:97], v[80:81], v[68:69], v[98:99] op_sel:[1,0,0]
	v_pk_fma_f32 v[90:91], v[80:81], v[66:67], v[90:91] op_sel:[1,0,0]
	s_waitcnt lgkmcnt(0)
	v_pk_fma_f32 v[92:93], v[80:81], v[72:73], v[92:93] op_sel:[1,0,0]
	v_pk_fma_f32 v[80:81], v[80:81], v[70:71], v[82:83] op_sel:[1,0,0]
	v_pk_fma_f32 v[82:83], v[74:75], v[68:69], v[94:95] op_sel:[1,0,0]
	v_pk_fma_f32 v[84:85], v[74:75], v[66:67], v[84:85] op_sel:[1,0,0]
	v_pk_fma_f32 v[88:89], v[74:75], v[72:73], v[88:89] op_sel:[1,0,0]
	v_pk_fma_f32 v[74:75], v[74:75], v[70:71], v[86:87] op_sel:[1,0,0]
	ds_read_b128 v[66:69], v167 offset:30720
	ds_read_b128 v[70:73], v167 offset:63488
	s_waitcnt lgkmcnt(1)
	v_pk_fma_f32 v[86:87], v[78:79], v[66:67], v[90:91] op_sel_hi:[0,1,1]
	v_pk_fma_f32 v[90:91], v[78:79], v[68:69], v[96:97] op_sel_hi:[0,1,1]
	s_waitcnt lgkmcnt(0)
	v_pk_fma_f32 v[80:81], v[78:79], v[70:71], v[80:81] op_sel_hi:[0,1,1]
	v_pk_fma_f32 v[92:93], v[78:79], v[72:73], v[92:93] op_sel_hi:[0,1,1]
	v_pk_fma_f32 v[84:85], v[76:77], v[66:67], v[84:85] op_sel_hi:[0,1,1]
	v_pk_fma_f32 v[82:83], v[76:77], v[68:69], v[82:83] op_sel_hi:[0,1,1]
	v_pk_fma_f32 v[74:75], v[76:77], v[70:71], v[74:75] op_sel_hi:[0,1,1]
	v_pk_fma_f32 v[88:89], v[76:77], v[72:73], v[88:89] op_sel_hi:[0,1,1]
	ds_read_b128 v[66:69], v167 offset:31744
	ds_read_b128 v[70:73], v167 offset:64512
	s_waitcnt lgkmcnt(1)
	v_pk_fma_f32 v[86:87], v[78:79], v[66:67], v[86:87] op_sel:[1,0,0]
	v_pk_fma_f32 v[90:91], v[78:79], v[68:69], v[90:91] op_sel:[1,0,0]
	s_waitcnt lgkmcnt(0)
	v_pk_fma_f32 v[92:93], v[78:79], v[72:73], v[92:93] op_sel:[1,0,0]
	v_pk_fma_f32 v[78:79], v[78:79], v[70:71], v[80:81] op_sel:[1,0,0]
	v_pk_fma_f32 v[70:71], v[76:77], v[70:71], v[74:75] op_sel:[1,0,0]
	v_cndmask_b32_e64 v75, v86, v87, s[6:7]
	v_pk_fma_f32 v[68:69], v[76:77], v[68:69], v[82:83] op_sel:[1,0,0]
	v_pk_fma_f32 v[66:67], v[76:77], v[66:67], v[84:85] op_sel:[1,0,0]
	v_pk_fma_f32 v[72:73], v[76:77], v[72:73], v[88:89] op_sel:[1,0,0]
	ds_bpermute_b32 v75, v1, v75
	v_cndmask_b32_e64 v76, v90, v91, s[6:7]
	ds_bpermute_b32 v76, v1, v76
	v_cndmask_b32_e64 v74, v87, v86, s[6:7]
	v_cndmask_b32_e64 v77, v78, v79, s[6:7]
	s_waitcnt lgkmcnt(1)
	v_add_f32_e32 v74, v74, v75
	v_cndmask_b32_e64 v75, v91, v90, s[6:7]
	s_waitcnt lgkmcnt(0)
	v_add_f32_e32 v75, v75, v76
	v_cndmask_b32_e64 v76, v79, v78, s[6:7]
	ds_bpermute_b32 v77, v1, v77
	v_cndmask_b32_e64 v78, v92, v93, s[6:7]
	ds_bpermute_b32 v78, v1, v78
	s_waitcnt lgkmcnt(1)
	v_add_f32_e32 v76, v76, v77
	v_cndmask_b32_e64 v77, v93, v92, s[6:7]
	s_waitcnt lgkmcnt(0)
	v_add_f32_e32 v77, v77, v78
	v_cndmask_b32_e64 v78, v67, v66, s[6:7]
	v_cndmask_b32_e64 v66, v66, v67, s[6:7]
	v_cndmask_b32_e64 v67, v69, v68, s[6:7]
	v_cndmask_b32_e64 v68, v68, v69, s[6:7]
	ds_bpermute_b32 v68, v1, v68
	v_cndmask_b32_e64 v69, v70, v71, s[6:7]
	ds_bpermute_b32 v69, v1, v69
	ds_bpermute_b32 v66, v1, v66
	s_waitcnt lgkmcnt(2)
	v_add_f32_e32 v67, v67, v68
	v_cndmask_b32_e64 v68, v71, v70, s[6:7]
	v_cndmask_b32_e64 v70, v72, v73, s[6:7]
	ds_bpermute_b32 v70, v1, v70
	v_cndmask_b32_e64 v71, v74, v75, s[8:9]
	s_waitcnt lgkmcnt(2)
	v_add_f32_e32 v68, v68, v69
	v_cndmask_b32_e64 v69, v73, v72, s[6:7]
	ds_bpermute_b32 v71, v135, v71
	v_cndmask_b32_e64 v72, v76, v77, s[8:9]
	ds_bpermute_b32 v72, v135, v72
	s_waitcnt lgkmcnt(2)
	v_add_f32_e32 v69, v69, v70
	v_cndmask_b32_e64 v70, v75, v74, s[8:9]
	v_add_f32_e32 v66, v78, v66
	s_waitcnt lgkmcnt(1)
	v_add_f32_e32 v70, v70, v71
	v_cndmask_b32_e64 v71, v77, v76, s[8:9]
	s_waitcnt lgkmcnt(0)
	v_add_f32_e32 v71, v71, v72
	v_cndmask_b32_e64 v72, v67, v66, s[8:9]
	v_cndmask_b32_e64 v66, v66, v67, s[8:9]
	v_cndmask_b32_e64 v67, v69, v68, s[8:9]
	v_cndmask_b32_e64 v68, v68, v69, s[8:9]
	ds_bpermute_b32 v66, v135, v66
	ds_bpermute_b32 v68, v135, v68
	v_cndmask_b32_e64 v69, v70, v71, s[10:11]
	ds_bpermute_b32 v69, v137, v69
	s_waitcnt lgkmcnt(2)
	v_add_f32_e32 v66, v72, v66
	s_waitcnt lgkmcnt(1)
	v_add_f32_e32 v67, v67, v68
	v_cndmask_b32_e64 v68, v71, v70, s[10:11]
	s_waitcnt lgkmcnt(0)
	v_add_f32_e32 v68, v68, v69
	v_cndmask_b32_e64 v69, v67, v66, s[10:11]
	v_cndmask_b32_e64 v66, v66, v67, s[10:11]
	ds_bpermute_b32 v66, v137, v66
	s_waitcnt lgkmcnt(0)
	v_add_f32_e32 v66, v69, v66
	v_cndmask_b32_e64 v67, v66, v68, s[12:13]
	v_cndmask_b32_e64 v66, v68, v66, s[12:13]
	ds_bpermute_b32 v66, v147, v66
	s_waitcnt lgkmcnt(0)
	v_add_f32_e32 v66, v67, v66
	ds_bpermute_b32 v67, v164, v66
	s_waitcnt lgkmcnt(0)
	v_add_f32_e32 v66, v66, v67
	ds_bpermute_b32 v67, v165, v66
	s_waitcnt lgkmcnt(0)
	v_add_f32_e32 v66, v66, v67
	s_nop 0
	v_readlane_b32 s74, v66, 0
	v_readlane_b32 s73, v66, 1
	v_readlane_b32 s72, v66, 2
	v_readlane_b32 s27, v66, 3
	v_readlane_b32 s26, v66, 4
	v_readlane_b32 s25, v66, 5
	v_readlane_b32 s24, v66, 6
	v_readlane_b32 s71, v66, 7
	v_readlane_b32 s86, v66, 8
	v_readlane_b32 s85, v66, 9
	v_readlane_b32 s84, v66, 10
	v_readlane_b32 s83, v66, 11
	v_readlane_b32 s82, v66, 12
	v_readlane_b32 s81, v66, 13
	v_readlane_b32 s80, v66, 14
	v_readlane_b32 s75, v66, 15
	s_and_saveexec_b64 s[68:69], s[4:5]
	s_cbranch_execz .LBB0_917
	v_mov_b32_e32 v66, s74
	v_cmp_gt_f32_e64 s[0:1], s73, v66
	v_mov_b32_e32 v67, s73
	v_mov_b32_e32 v69, s72
	v_cndmask_b32_e64 v68, v66, v67, s[0:1]
	v_cmp_gt_f32_e64 s[14:15], s72, v68
	v_mov_b32_e32 v70, s27
	v_mov_b32_e32 v71, s26
	v_cndmask_b32_e64 v68, v68, v69, s[14:15]
	v_cmp_gt_f32_e64 s[16:17], s27, v68
	v_mov_b32_e32 v72, s25
	v_mov_b32_e32 v73, s24
	v_cndmask_b32_e64 v68, v68, v70, s[16:17]
	v_cmp_gt_f32_e64 s[18:19], s26, v68
	s_add_i32 s79, s77, s37
	s_add_i32 s79, s79, 0x10000
	v_cndmask_b32_e64 v68, v68, v71, s[18:19]
	v_cmp_gt_f32_e64 s[20:21], s25, v68
	v_cndmask_b32_e64 v74, 0, 1, s[0:1]
	v_mov_b32_e32 v75, s80
	v_cndmask_b32_e64 v68, v68, v72, s[20:21]
	v_cmp_gt_f32_e64 s[22:23], s24, v68
	s_nop 1
	v_cndmask_b32_e64 v68, v68, v73, s[22:23]
	v_cmp_ngt_f32_e32 vcc, s71, v68
	s_and_b64 s[90:91], s[22:23], vcc
	s_and_b64 s[0:1], s[14:15], exec
	v_readfirstlane_b32 s0, v74
	s_cselect_b32 s14, 2, s0
	s_and_b64 s[0:1], s[16:17], exec
	s_cselect_b32 s14, 3, s14
	s_and_b64 s[0:1], s[18:19], exec
	s_cselect_b32 s14, 4, s14
	s_and_b64 s[0:1], s[20:21], exec
	s_cselect_b32 s14, 5, s14
	s_and_b64 s[0:1], s[22:23], exec
	s_cselect_b32 s14, 6, s14
	s_and_b64 s[0:1], vcc, exec
	s_cselect_b32 s70, s14, 7
	s_cmp_lg_u32 s70, 5
	s_cselect_b64 s[92:93], -1, 0
	s_cmp_lg_u32 s70, 4
	s_cselect_b64 s[22:23], -1, 0
	s_cmp_lg_u32 s70, 3
	s_cselect_b64 s[20:21], -1, 0
	s_cmp_lg_u32 s70, 2
	s_cselect_b64 s[18:19], -1, 0
	s_cmp_lg_u32 s70, 1
	s_cselect_b64 s[16:17], -1, 0
	s_cmp_eq_u32 s70, 0
	s_cselect_b64 s[14:15], -1, 0
	v_cmp_nlg_f32_e64 s[0:1], s74, v180
	s_or_b64 s[0:1], s[14:15], s[0:1]
	v_mov_b32_e32 v74, s81
	v_cndmask_b32_e64 v66, v66, v180, s[0:1]
	v_cmp_gt_f32_e64 s[14:15], s73, v66
	s_and_b64 s[14:15], s[16:17], s[14:15]
	s_nop 0
	v_cndmask_b32_e64 v66, v66, v67, s[14:15]
	v_cmp_gt_f32_e64 s[16:17], s72, v66
	s_and_b64 s[16:17], s[18:19], s[16:17]
	v_mov_b32_e32 v67, s71
	v_cndmask_b32_e64 v66, v66, v69, s[16:17]
	v_cmp_gt_f32_e64 s[18:19], s27, v66
	s_and_b64 s[18:19], s[20:21], s[18:19]
	v_cndmask_b32_e64 v69, 0, -1, s[0:1]
	v_cndmask_b32_e64 v66, v66, v70, s[18:19]
	v_cmp_gt_f32_e64 s[20:21], s26, v66
	s_and_b64 s[20:21], s[22:23], s[20:21]
	s_nop 0
	v_cndmask_b32_e64 v66, v66, v71, s[20:21]
	v_cmp_gt_f32_e64 s[22:23], s25, v66
	s_and_b64 s[22:23], s[92:93], s[22:23]
	s_nop 0
	v_cndmask_b32_e64 v66, v66, v72, s[22:23]
	v_cmp_ngt_f32_e64 s[24:25], s24, v66
	s_or_b64 s[24:25], s[90:91], s[24:25]
	s_nop 0
	v_cndmask_b32_e64 v66, v73, v66, s[24:25]
	v_cmp_gt_f32_e64 s[26:27], s71, v66
	s_and_b64 s[26:27], vcc, s[26:27]
	v_mov_b32_e32 v73, s82
	v_cndmask_b32_e64 v66, v66, v67, s[26:27]
	v_cndmask_b32_e32 v67, v67, v68, vcc
	v_sub_f32_e32 v66, v66, v67
	v_mul_f32_e32 v66, 0x3fb8aa3b, v66
	v_exp_f32_e32 v66, v66
	s_nop 0
	v_add_f32_e32 v66, 1.0, v66
	v_div_scale_f32 v67, s[0:1], v66, v66, 1.0
	v_rcp_f32_e32 v68, v67
	v_readfirstlane_b32 s0, v69
	s_lshl_b32 s71, s0, 8
	s_and_b64 s[0:1], s[14:15], exec
	v_fma_f32 v70, -v67, v68, 1.0
	s_cselect_b32 s14, 0x100, s71
	s_and_b64 s[0:1], s[16:17], exec
	v_fmac_f32_e32 v68, v70, v68
	v_div_scale_f32 v70, vcc, 1.0, v66, 1.0
	s_cselect_b32 s14, 0x200, s14
	s_and_b64 s[0:1], s[18:19], exec
	v_mul_f32_e32 v71, v70, v68
	s_cselect_b32 s14, 0x300, s14
	s_and_b64 s[0:1], s[20:21], exec
	v_fma_f32 v72, -v67, v71, v70
	s_cselect_b32 s14, 0x400, s14
	s_and_b64 s[0:1], s[22:23], exec
	v_fmac_f32_e32 v71, v72, v68
	s_cselect_b32 s14, 0x500, s14
	s_and_b64 s[0:1], s[24:25], exec
	v_fma_f32 v67, -v67, v71, v70
	s_cselect_b32 s14, s14, 0x600
	s_and_b64 s[0:1], s[26:27], exec
	v_div_fmas_f32 v67, v67, v68, v71
	s_cselect_b32 s0, 0x700, s14
	v_mov_b32_e32 v68, s86
	s_add_i32 s74, s0, s70
	v_cmp_gt_f32_e64 s[0:1], s85, v68
	v_mov_b32_e32 v69, s85
	v_mov_b32_e32 v71, s84
	v_cndmask_b32_e64 v70, v68, v69, s[0:1]
	v_cmp_gt_f32_e64 s[14:15], s84, v70
	v_mov_b32_e32 v72, s83
	s_add_u32 s72, s46, s66
	v_cndmask_b32_e64 v70, v70, v71, s[14:15]
	v_cmp_gt_f32_e64 s[16:17], s83, v70
	s_addc_u32 s73, s47, s67
	s_add_u32 s70, s46, s64
	v_cndmask_b32_e64 v70, v70, v72, s[16:17]
	v_cmp_gt_f32_e64 s[18:19], s82, v70
	s_addc_u32 s71, s47, s65
	v_cndmask_b32_e64 v76, 0, 1, s[0:1]
	v_cndmask_b32_e64 v70, v70, v73, s[18:19]
	v_cmp_gt_f32_e64 s[20:21], s81, v70
	v_div_fixup_f32 v66, v67, v66, 1.0
	v_sub_f32_e32 v67, 1.0, v66
	v_cndmask_b32_e64 v70, v70, v74, s[20:21]
	v_cmp_gt_f32_e64 s[22:23], s80, v70
	s_nop 1
	v_cndmask_b32_e64 v70, v70, v75, s[22:23]
	v_cmp_ngt_f32_e32 vcc, s75, v70
	s_and_b64 s[26:27], s[22:23], vcc
	s_and_b64 s[0:1], s[14:15], exec
	v_readfirstlane_b32 s0, v76
	s_cselect_b32 s14, 2, s0
	s_and_b64 s[0:1], s[16:17], exec
	s_cselect_b32 s14, 3, s14
	s_and_b64 s[0:1], s[18:19], exec
	s_cselect_b32 s14, 4, s14
	s_and_b64 s[0:1], s[20:21], exec
	s_cselect_b32 s14, 5, s14
	s_and_b64 s[0:1], s[22:23], exec
	s_cselect_b32 s14, 6, s14
	s_and_b64 s[0:1], vcc, exec
	s_cselect_b32 s87, s14, 7
	s_cmp_lg_u32 s87, 5
	s_cselect_b64 s[24:25], -1, 0
	s_cmp_lg_u32 s87, 4
	s_cselect_b64 s[22:23], -1, 0
	s_cmp_lg_u32 s87, 3
	s_cselect_b64 s[20:21], -1, 0
	s_cmp_lg_u32 s87, 2
	s_cselect_b64 s[18:19], -1, 0
	s_cmp_lg_u32 s87, 1
	s_cselect_b64 s[16:17], -1, 0
	s_cmp_eq_u32 s87, 0
	s_cselect_b64 s[14:15], -1, 0
	v_cmp_nlg_f32_e64 s[0:1], s86, v180
	s_or_b64 s[0:1], s[14:15], s[0:1]
	s_nop 0
	v_cndmask_b32_e64 v68, v68, v180, s[0:1]
	v_cmp_gt_f32_e64 s[14:15], s85, v68
	s_and_b64 s[14:15], s[16:17], s[14:15]
	s_nop 0
	v_cndmask_b32_e64 v68, v68, v69, s[14:15]
	v_cmp_gt_f32_e64 s[16:17], s84, v68
	s_and_b64 s[16:17], s[18:19], s[16:17]
	v_mov_b32_e32 v69, s75
	v_cndmask_b32_e64 v68, v68, v71, s[16:17]
	v_cmp_gt_f32_e64 s[18:19], s83, v68
	s_and_b64 s[18:19], s[20:21], s[18:19]
	v_cndmask_b32_e64 v71, 0, -1, s[0:1]
	v_cndmask_b32_e64 v68, v68, v72, s[18:19]
	v_cmp_gt_f32_e64 s[20:21], s82, v68
	s_and_b64 s[20:21], s[22:23], s[20:21]
	s_nop 0
	v_cndmask_b32_e64 v68, v68, v73, s[20:21]
	v_cmp_gt_f32_e64 s[22:23], s81, v68
	s_and_b64 s[22:23], s[24:25], s[22:23]
	s_nop 0
	v_cndmask_b32_e64 v68, v68, v74, s[22:23]
	v_cmp_ngt_f32_e64 s[24:25], s80, v68
	s_or_b64 s[24:25], s[26:27], s[24:25]
	s_nop 0
	v_cndmask_b32_e64 v68, v75, v68, s[24:25]
	v_cmp_gt_f32_e64 s[26:27], s75, v68
	s_and_b64 s[26:27], vcc, s[26:27]
	s_nop 0
	v_cndmask_b32_e64 v68, v68, v69, s[26:27]
	v_cndmask_b32_e32 v69, v69, v70, vcc
	v_sub_f32_e32 v68, v68, v69
	v_mul_f32_e32 v68, 0x3fb8aa3b, v68
	v_exp_f32_e32 v68, v68
	s_nop 0
	v_add_f32_e32 v68, 1.0, v68
	v_div_scale_f32 v69, s[0:1], v68, v68, 1.0
	v_rcp_f32_e32 v70, v69
	v_readfirstlane_b32 s0, v71
	s_lshl_b32 s75, s0, 8
	s_and_b64 s[0:1], s[14:15], exec
	v_fma_f32 v72, -v69, v70, 1.0
	v_fmac_f32_e32 v70, v72, v70
	v_div_scale_f32 v72, vcc, 1.0, v68, 1.0
	s_cselect_b32 s14, 0x100, s75
	s_and_b64 s[0:1], s[16:17], exec
	v_mul_f32_e32 v73, v72, v70
	s_cselect_b32 s14, 0x200, s14
	s_and_b64 s[0:1], s[18:19], exec
	v_fma_f32 v74, -v69, v73, v72
	s_cselect_b32 s14, 0x300, s14
	s_and_b64 s[0:1], s[20:21], exec
	v_fmac_f32_e32 v73, v74, v70
	s_cselect_b32 s14, 0x400, s14
	s_and_b64 s[0:1], s[22:23], exec
	v_fma_f32 v69, -v69, v73, v72
	s_cselect_b32 s14, 0x500, s14
	s_and_b64 s[0:1], s[24:25], exec
	v_div_fmas_f32 v69, v69, v70, v73
	s_cselect_b32 s14, s14, 0x600
	s_and_b64 s[0:1], s[26:27], exec
	v_div_fixup_f32 v68, v69, v68, 1.0
	s_cselect_b32 s0, 0x700, s14
	s_add_i32 s75, s0, s87
	v_sub_f32_e32 v69, 1.0, v68
	v_mov_b64_e32 v[70:71], s[74:75]
	global_store_dwordx4 v139, v[66:69], s[70:71] offset:-8
	global_store_dwordx2 v177, v[70:71], s[72:73]
	s_nop 0
	v_mov_b32_e32 v66, s79
	ds_write_b64 v66, v[70:71]
	s_branch .LBB0_917

.LBB0_1087:
	v_pk_mul_f32 v[164:165], v[126:127], s[12:13] op_sel_hi:[1,0]
	v_pk_mul_f32 v[168:169], v[122:123], s[12:13] op_sel_hi:[1,0]
	v_exp_f32_e32 v164, v164
	v_exp_f32_e32 v165, v165
	v_exp_f32_e32 v168, v168
	v_exp_f32_e32 v169, v169
	v_pk_mul_f32 v[160:161], v[128:129], s[12:13] op_sel_hi:[1,0]
	v_pk_mul_f32 v[166:167], v[124:125], s[12:13] op_sel_hi:[1,0]
	v_pk_fma_f32 v[164:165], v[164:165], s[14:15], s[14:15] op_sel_hi:[1,0,0]
	v_exp_f32_e32 v160, v160
	v_exp_f32_e32 v161, v161
	v_exp_f32_e32 v166, v166
	v_exp_f32_e32 v167, v167
	v_rcp_f32_e32 v164, v164
	v_rcp_f32_e32 v165, v165
	v_pk_fma_f32 v[168:169], v[168:169], s[14:15], s[14:15] op_sel_hi:[1,0,0]
	v_pk_mul_f32 v[118:119], v[126:127], v[118:119]
	v_rcp_f32_e32 v168, v168
	v_rcp_f32_e32 v169, v169
	v_pk_fma_f32 v[160:161], v[160:161], s[14:15], s[14:15] op_sel_hi:[1,0,0]
	v_pk_fma_f32 v[166:167], v[166:167], s[14:15], s[14:15] op_sel_hi:[1,0,0]
	v_pk_mul_f32 v[118:119], v[118:119], v[164:165]
	v_pk_mul_f32 v[114:115], v[122:123], v[114:115]
	v_rcp_f32_e32 v160, v160
	v_rcp_f32_e32 v161, v161
	v_rcp_f32_e32 v166, v166
	v_rcp_f32_e32 v167, v167
	v_pk_mul_f32 v[114:115], v[114:115], v[168:169]
	v_med3_f32 v122, v118, s56, v157
	v_med3_f32 v119, v119, s56, v157
	s_nop 0
	v_cvt_pk_fp8_f32 v118, v122, v119
	v_med3_f32 v114, v114, s56, v157
	v_med3_f32 v115, v115, s56, v157
	s_nop 0
	v_cvt_pk_fp8_f32 v119, v114, v115
	v_pk_mul_f32 v[120:121], v[128:129], v[120:121]
	v_pk_mul_f32 v[116:117], v[124:125], v[116:117]
	v_pk_mul_f32 v[120:121], v[120:121], v[160:161]
	v_pk_mul_f32 v[116:117], v[116:117], v[166:167]
	v_med3_f32 v120, v120, s56, v157
	v_med3_f32 v121, v121, s56, v157
	v_med3_f32 v114, v116, s56, v157
	v_med3_f32 v115, v117, s56, v157
	v_pk_mul_f32 v[116:117], v[110:111], s[12:13] op_sel_hi:[1,0]
	v_cvt_pk_fp8_f32 v118, v120, v121 op_sel:[0,0,1]
	v_cvt_pk_fp8_f32 v119, v114, v115 op_sel:[0,0,1]
	v_exp_f32_e32 v116, v116
	v_exp_f32_e32 v117, v117
	v_pk_mul_f32 v[120:121], v[106:107], s[12:13] op_sel_hi:[1,0]
	v_lshl_add_u32 v158, s24, 8, v1
	v_lshl_or_b32 v148, s58, 7, v147
	v_mov_b64_e32 v[150:151], s[6:7]
	v_exp_f32_e32 v120, v120
	v_exp_f32_e32 v121, v121
	v_ashrrev_i32_e32 v149, 31, v148
	v_mad_i64_i32 v[114:115], s[26:27], v158, s55, v[150:151]
	v_lshl_add_u64 v[114:115], v[114:115], 0, v[148:149]
	global_store_dwordx2 v[114:115], v[118:119], off
	v_pk_mul_f32 v[114:115], v[112:113], s[12:13] op_sel_hi:[1,0]
	v_pk_mul_f32 v[118:119], v[108:109], s[12:13] op_sel_hi:[1,0]
	v_pk_fma_f32 v[116:117], v[116:117], s[14:15], s[14:15] op_sel_hi:[1,0,0]
	v_exp_f32_e32 v114, v114
	v_exp_f32_e32 v115, v115
	v_exp_f32_e32 v118, v118
	v_exp_f32_e32 v119, v119
	v_rcp_f32_e32 v116, v116
	v_rcp_f32_e32 v117, v117
	v_pk_fma_f32 v[120:121], v[120:121], s[14:15], s[14:15] op_sel_hi:[1,0,0]
	v_pk_mul_f32 v[102:103], v[110:111], v[102:103]
	v_rcp_f32_e32 v120, v120
	v_rcp_f32_e32 v121, v121
	v_pk_fma_f32 v[114:115], v[114:115], s[14:15], s[14:15] op_sel_hi:[1,0,0]
	v_pk_fma_f32 v[118:119], v[118:119], s[14:15], s[14:15] op_sel_hi:[1,0,0]
	v_pk_mul_f32 v[102:103], v[102:103], v[116:117]
	v_pk_mul_f32 v[98:99], v[106:107], v[98:99]
	v_rcp_f32_e32 v114, v114
	v_rcp_f32_e32 v115, v115
	v_rcp_f32_e32 v118, v118
	v_rcp_f32_e32 v119, v119
	v_pk_mul_f32 v[98:99], v[98:99], v[120:121]
	v_med3_f32 v106, v102, s56, v157
	v_med3_f32 v103, v103, s56, v157
	s_nop 0
	v_cvt_pk_fp8_f32 v102, v106, v103
	v_med3_f32 v98, v98, s56, v157
	v_med3_f32 v99, v99, s56, v157
	s_nop 0
	v_cvt_pk_fp8_f32 v103, v98, v99
	v_pk_mul_f32 v[104:105], v[112:113], v[104:105]
	v_pk_mul_f32 v[100:101], v[108:109], v[100:101]
	v_pk_mul_f32 v[104:105], v[104:105], v[114:115]
	v_pk_mul_f32 v[100:101], v[100:101], v[118:119]
	v_med3_f32 v104, v104, s56, v157
	v_med3_f32 v105, v105, s56, v157
	v_med3_f32 v98, v100, s56, v157
	v_med3_f32 v99, v101, s56, v157
	v_pk_mul_f32 v[100:101], v[94:95], s[12:13] op_sel_hi:[1,0]
	v_cvt_pk_fp8_f32 v102, v104, v105 op_sel:[0,0,1]
	v_cvt_pk_fp8_f32 v103, v98, v99 op_sel:[0,0,1]
	v_exp_f32_e32 v100, v100
	v_exp_f32_e32 v101, v101
	v_pk_mul_f32 v[104:105], v[90:91], s[12:13] op_sel_hi:[1,0]
	v_or_b32_e32 v122, 16, v158
	v_exp_f32_e32 v104, v104
	v_exp_f32_e32 v105, v105
	v_mad_i64_i32 v[98:99], s[26:27], v122, s55, v[150:151]
	v_lshl_add_u64 v[98:99], v[98:99], 0, v[148:149]
	global_store_dwordx2 v[98:99], v[102:103], off
	v_pk_mul_f32 v[98:99], v[96:97], s[12:13] op_sel_hi:[1,0]
	v_pk_mul_f32 v[102:103], v[92:93], s[12:13] op_sel_hi:[1,0]
	v_pk_fma_f32 v[100:101], v[100:101], s[14:15], s[14:15] op_sel_hi:[1,0,0]
	v_exp_f32_e32 v98, v98
	v_exp_f32_e32 v99, v99
	v_exp_f32_e32 v102, v102
	v_exp_f32_e32 v103, v103
	v_rcp_f32_e32 v100, v100
	v_rcp_f32_e32 v101, v101
	v_pk_fma_f32 v[104:105], v[104:105], s[14:15], s[14:15] op_sel_hi:[1,0,0]
	v_pk_mul_f32 v[86:87], v[94:95], v[86:87]
	v_rcp_f32_e32 v104, v104
	v_rcp_f32_e32 v105, v105
	v_pk_fma_f32 v[98:99], v[98:99], s[14:15], s[14:15] op_sel_hi:[1,0,0]
	v_pk_fma_f32 v[102:103], v[102:103], s[14:15], s[14:15] op_sel_hi:[1,0,0]
	v_pk_mul_f32 v[86:87], v[86:87], v[100:101]
	v_pk_mul_f32 v[82:83], v[90:91], v[82:83]
	v_rcp_f32_e32 v98, v98
	v_rcp_f32_e32 v99, v99
	v_rcp_f32_e32 v102, v102
	v_rcp_f32_e32 v103, v103
	v_pk_mul_f32 v[82:83], v[82:83], v[104:105]
	v_med3_f32 v90, v86, s56, v157
	v_med3_f32 v87, v87, s56, v157
	s_nop 0
	v_cvt_pk_fp8_f32 v86, v90, v87
	v_med3_f32 v82, v82, s56, v157
	v_med3_f32 v83, v83, s56, v157
	s_nop 0
	v_cvt_pk_fp8_f32 v87, v82, v83
	v_pk_mul_f32 v[88:89], v[96:97], v[88:89]
	v_pk_mul_f32 v[84:85], v[92:93], v[84:85]
	v_pk_mul_f32 v[88:89], v[88:89], v[98:99]
	v_pk_mul_f32 v[84:85], v[84:85], v[102:103]
	v_med3_f32 v88, v88, s56, v157
	v_med3_f32 v89, v89, s56, v157
	v_med3_f32 v82, v84, s56, v157
	v_med3_f32 v83, v85, s56, v157
	v_pk_mul_f32 v[84:85], v[78:79], s[12:13] op_sel_hi:[1,0]
	v_cvt_pk_fp8_f32 v86, v88, v89 op_sel:[0,0,1]
	v_cvt_pk_fp8_f32 v87, v82, v83 op_sel:[0,0,1]
	v_exp_f32_e32 v84, v84
	v_exp_f32_e32 v85, v85
	v_pk_mul_f32 v[88:89], v[74:75], s[12:13] op_sel_hi:[1,0]
	v_or_b32_e32 v106, 32, v158
	v_exp_f32_e32 v88, v88
	v_exp_f32_e32 v89, v89
	v_mad_i64_i32 v[82:83], s[26:27], v106, s55, v[150:151]
	v_lshl_add_u64 v[82:83], v[82:83], 0, v[148:149]
	global_store_dwordx2 v[82:83], v[86:87], off
	v_pk_mul_f32 v[82:83], v[80:81], s[12:13] op_sel_hi:[1,0]
	v_pk_mul_f32 v[86:87], v[76:77], s[12:13] op_sel_hi:[1,0]
	v_pk_fma_f32 v[84:85], v[84:85], s[14:15], s[14:15] op_sel_hi:[1,0,0]
	v_exp_f32_e32 v82, v82
	v_exp_f32_e32 v83, v83
	v_exp_f32_e32 v86, v86
	v_exp_f32_e32 v87, v87
	v_rcp_f32_e32 v84, v84
	v_rcp_f32_e32 v85, v85
	v_pk_fma_f32 v[88:89], v[88:89], s[14:15], s[14:15] op_sel_hi:[1,0,0]
	v_pk_mul_f32 v[70:71], v[78:79], v[70:71]
	v_rcp_f32_e32 v88, v88
	v_rcp_f32_e32 v89, v89
	v_pk_fma_f32 v[82:83], v[82:83], s[14:15], s[14:15] op_sel_hi:[1,0,0]
	v_pk_fma_f32 v[86:87], v[86:87], s[14:15], s[14:15] op_sel_hi:[1,0,0]
	v_pk_mul_f32 v[70:71], v[70:71], v[84:85]
	v_pk_mul_f32 v[66:67], v[74:75], v[66:67]
	v_rcp_f32_e32 v82, v82
	v_rcp_f32_e32 v83, v83
	v_rcp_f32_e32 v86, v86
	v_rcp_f32_e32 v87, v87
	v_pk_mul_f32 v[66:67], v[66:67], v[88:89]
	v_med3_f32 v74, v70, s56, v157
	v_med3_f32 v71, v71, s56, v157
	s_nop 0
	v_cvt_pk_fp8_f32 v70, v74, v71
	v_med3_f32 v66, v66, s56, v157
	v_med3_f32 v67, v67, s56, v157
	s_nop 0
	v_cvt_pk_fp8_f32 v71, v66, v67
	v_pk_mul_f32 v[72:73], v[80:81], v[72:73]
	v_pk_mul_f32 v[68:69], v[76:77], v[68:69]
	v_pk_mul_f32 v[72:73], v[72:73], v[82:83]
	v_pk_mul_f32 v[68:69], v[68:69], v[86:87]
	v_med3_f32 v72, v72, s56, v157
	v_med3_f32 v73, v73, s56, v157
	v_med3_f32 v66, v68, s56, v157
	v_med3_f32 v67, v69, s56, v157
	v_pk_mul_f32 v[68:69], v[62:63], s[12:13] op_sel_hi:[1,0]
	v_cvt_pk_fp8_f32 v70, v72, v73 op_sel:[0,0,1]
	v_cvt_pk_fp8_f32 v71, v66, v67 op_sel:[0,0,1]
	v_exp_f32_e32 v68, v68
	v_exp_f32_e32 v69, v69
	v_pk_mul_f32 v[72:73], v[58:59], s[12:13] op_sel_hi:[1,0]
	v_or_b32_e32 v90, 48, v158
	v_exp_f32_e32 v72, v72
	v_exp_f32_e32 v73, v73
	v_mad_i64_i32 v[66:67], s[26:27], v90, s55, v[150:151]
	v_lshl_add_u64 v[66:67], v[66:67], 0, v[148:149]
	global_store_dwordx2 v[66:67], v[70:71], off
	v_pk_mul_f32 v[66:67], v[64:65], s[12:13] op_sel_hi:[1,0]
	v_pk_mul_f32 v[70:71], v[60:61], s[12:13] op_sel_hi:[1,0]
	v_pk_fma_f32 v[68:69], v[68:69], s[14:15], s[14:15] op_sel_hi:[1,0,0]
	v_exp_f32_e32 v66, v66
	v_exp_f32_e32 v67, v67
	v_exp_f32_e32 v70, v70
	v_exp_f32_e32 v71, v71
	v_rcp_f32_e32 v68, v68
	v_rcp_f32_e32 v69, v69
	v_pk_fma_f32 v[72:73], v[72:73], s[14:15], s[14:15] op_sel_hi:[1,0,0]
	v_pk_mul_f32 v[54:55], v[62:63], v[54:55]
	v_rcp_f32_e32 v72, v72
	v_rcp_f32_e32 v73, v73
	v_pk_fma_f32 v[66:67], v[66:67], s[14:15], s[14:15] op_sel_hi:[1,0,0]
	v_pk_fma_f32 v[70:71], v[70:71], s[14:15], s[14:15] op_sel_hi:[1,0,0]
	v_pk_mul_f32 v[54:55], v[54:55], v[68:69]
	v_pk_mul_f32 v[50:51], v[58:59], v[50:51]
	v_rcp_f32_e32 v66, v66
	v_rcp_f32_e32 v67, v67
	v_rcp_f32_e32 v70, v70
	v_rcp_f32_e32 v71, v71
	v_pk_mul_f32 v[50:51], v[50:51], v[72:73]
	v_med3_f32 v58, v54, s56, v157
	v_med3_f32 v55, v55, s56, v157
	s_nop 0
	v_cvt_pk_fp8_f32 v54, v58, v55
	v_med3_f32 v50, v50, s56, v157
	v_med3_f32 v51, v51, s56, v157
	s_nop 0
	v_cvt_pk_fp8_f32 v55, v50, v51
	v_pk_mul_f32 v[56:57], v[64:65], v[56:57]
	v_pk_mul_f32 v[52:53], v[60:61], v[52:53]
	v_pk_mul_f32 v[56:57], v[56:57], v[66:67]
	v_pk_mul_f32 v[52:53], v[52:53], v[70:71]
	v_med3_f32 v56, v56, s56, v157
	v_med3_f32 v57, v57, s56, v157
	v_med3_f32 v50, v52, s56, v157
	v_med3_f32 v51, v53, s56, v157
	v_pk_mul_f32 v[52:53], v[46:47], s[12:13] op_sel_hi:[1,0]
	v_cvt_pk_fp8_f32 v54, v56, v57 op_sel:[0,0,1]
	v_cvt_pk_fp8_f32 v55, v50, v51 op_sel:[0,0,1]
	v_exp_f32_e32 v52, v52
	v_exp_f32_e32 v53, v53
	v_pk_mul_f32 v[56:57], v[42:43], s[12:13] op_sel_hi:[1,0]
	v_add_u32_e32 v74, 0x80, v158
	v_exp_f32_e32 v56, v56
	v_exp_f32_e32 v57, v57
	v_mad_i64_i32 v[50:51], s[26:27], v74, s55, v[150:151]
	v_lshl_add_u64 v[50:51], v[50:51], 0, v[148:149]
	global_store_dwordx2 v[50:51], v[54:55], off
	v_pk_mul_f32 v[50:51], v[48:49], s[12:13] op_sel_hi:[1,0]
	v_pk_mul_f32 v[54:55], v[44:45], s[12:13] op_sel_hi:[1,0]
	v_pk_fma_f32 v[52:53], v[52:53], s[14:15], s[14:15] op_sel_hi:[1,0,0]
	v_exp_f32_e32 v50, v50
	v_exp_f32_e32 v51, v51
	v_exp_f32_e32 v54, v54
	v_exp_f32_e32 v55, v55
	v_rcp_f32_e32 v52, v52
	v_rcp_f32_e32 v53, v53
	v_pk_fma_f32 v[56:57], v[56:57], s[14:15], s[14:15] op_sel_hi:[1,0,0]
	v_pk_mul_f32 v[38:39], v[46:47], v[38:39]
	v_rcp_f32_e32 v56, v56
	v_rcp_f32_e32 v57, v57
	v_pk_fma_f32 v[50:51], v[50:51], s[14:15], s[14:15] op_sel_hi:[1,0,0]
	v_pk_fma_f32 v[54:55], v[54:55], s[14:15], s[14:15] op_sel_hi:[1,0,0]
	v_pk_mul_f32 v[38:39], v[38:39], v[52:53]
	v_pk_mul_f32 v[34:35], v[42:43], v[34:35]
	v_rcp_f32_e32 v50, v50
	v_rcp_f32_e32 v51, v51
	v_rcp_f32_e32 v54, v54
	v_rcp_f32_e32 v55, v55
	v_pk_mul_f32 v[34:35], v[34:35], v[56:57]
	v_med3_f32 v42, v38, s56, v157
	v_med3_f32 v39, v39, s56, v157
	s_nop 0
	v_cvt_pk_fp8_f32 v38, v42, v39
	v_med3_f32 v34, v34, s56, v157
	v_med3_f32 v35, v35, s56, v157
	s_nop 0
	v_cvt_pk_fp8_f32 v39, v34, v35
	v_pk_mul_f32 v[40:41], v[48:49], v[40:41]
	v_pk_mul_f32 v[36:37], v[44:45], v[36:37]
	v_pk_mul_f32 v[40:41], v[40:41], v[50:51]
	v_pk_mul_f32 v[36:37], v[36:37], v[54:55]
	v_med3_f32 v40, v40, s56, v157
	v_med3_f32 v41, v41, s56, v157
	v_med3_f32 v34, v36, s56, v157
	v_med3_f32 v35, v37, s56, v157
	v_pk_mul_f32 v[36:37], v[30:31], s[12:13] op_sel_hi:[1,0]
	v_cvt_pk_fp8_f32 v38, v40, v41 op_sel:[0,0,1]
	v_cvt_pk_fp8_f32 v39, v34, v35 op_sel:[0,0,1]
	v_exp_f32_e32 v36, v36
	v_exp_f32_e32 v37, v37
	v_pk_mul_f32 v[40:41], v[26:27], s[12:13] op_sel_hi:[1,0]
	v_add_u32_e32 v58, 0x90, v158
	v_exp_f32_e32 v40, v40
	v_exp_f32_e32 v41, v41
	v_mad_i64_i32 v[34:35], s[26:27], v58, s55, v[150:151]
	v_lshl_add_u64 v[34:35], v[34:35], 0, v[148:149]
	global_store_dwordx2 v[34:35], v[38:39], off
	v_pk_mul_f32 v[34:35], v[32:33], s[12:13] op_sel_hi:[1,0]
	v_pk_mul_f32 v[38:39], v[28:29], s[12:13] op_sel_hi:[1,0]
	v_pk_fma_f32 v[36:37], v[36:37], s[14:15], s[14:15] op_sel_hi:[1,0,0]
	v_exp_f32_e32 v34, v34
	v_exp_f32_e32 v35, v35
	v_exp_f32_e32 v38, v38
	v_exp_f32_e32 v39, v39
	v_rcp_f32_e32 v36, v36
	v_rcp_f32_e32 v37, v37
	v_pk_fma_f32 v[40:41], v[40:41], s[14:15], s[14:15] op_sel_hi:[1,0,0]
	v_pk_mul_f32 v[22:23], v[30:31], v[22:23]
	v_rcp_f32_e32 v40, v40
	v_rcp_f32_e32 v41, v41
	v_pk_fma_f32 v[34:35], v[34:35], s[14:15], s[14:15] op_sel_hi:[1,0,0]
	v_pk_fma_f32 v[38:39], v[38:39], s[14:15], s[14:15] op_sel_hi:[1,0,0]
	v_pk_mul_f32 v[22:23], v[22:23], v[36:37]
	v_pk_mul_f32 v[18:19], v[26:27], v[18:19]
	v_rcp_f32_e32 v34, v34
	v_rcp_f32_e32 v35, v35
	v_rcp_f32_e32 v38, v38
	v_rcp_f32_e32 v39, v39
	v_pk_mul_f32 v[18:19], v[18:19], v[40:41]
	v_med3_f32 v26, v22, s56, v157
	v_med3_f32 v23, v23, s56, v157
	s_nop 0
	v_cvt_pk_fp8_f32 v22, v26, v23
	v_med3_f32 v18, v18, s56, v157
	v_med3_f32 v19, v19, s56, v157
	s_nop 0
	v_cvt_pk_fp8_f32 v23, v18, v19
	v_pk_mul_f32 v[24:25], v[32:33], v[24:25]
	v_pk_mul_f32 v[20:21], v[28:29], v[20:21]
	v_pk_mul_f32 v[24:25], v[24:25], v[34:35]
	v_pk_mul_f32 v[20:21], v[20:21], v[38:39]
	v_med3_f32 v24, v24, s56, v157
	v_med3_f32 v25, v25, s56, v157
	v_med3_f32 v18, v20, s56, v157
	v_med3_f32 v19, v21, s56, v157
	v_pk_mul_f32 v[20:21], v[14:15], s[12:13] op_sel_hi:[1,0]
	v_cvt_pk_fp8_f32 v22, v24, v25 op_sel:[0,0,1]
	v_cvt_pk_fp8_f32 v23, v18, v19 op_sel:[0,0,1]
	v_exp_f32_e32 v20, v20
	v_exp_f32_e32 v21, v21
	v_pk_mul_f32 v[24:25], v[10:11], s[12:13] op_sel_hi:[1,0]
	v_add_u32_e32 v42, 0xa0, v158
	v_exp_f32_e32 v24, v24
	v_exp_f32_e32 v25, v25
	v_mad_i64_i32 v[18:19], s[26:27], v42, s55, v[150:151]
	v_lshl_add_u64 v[18:19], v[18:19], 0, v[148:149]
	global_store_dwordx2 v[18:19], v[22:23], off
	v_pk_mul_f32 v[18:19], v[16:17], s[12:13] op_sel_hi:[1,0]
	v_pk_mul_f32 v[22:23], v[12:13], s[12:13] op_sel_hi:[1,0]
	v_pk_fma_f32 v[20:21], v[20:21], s[14:15], s[14:15] op_sel_hi:[1,0,0]
	v_exp_f32_e32 v18, v18
	v_exp_f32_e32 v19, v19
	v_exp_f32_e32 v22, v22
	v_exp_f32_e32 v23, v23
	v_rcp_f32_e32 v20, v20
	v_rcp_f32_e32 v21, v21
	v_pk_fma_f32 v[24:25], v[24:25], s[14:15], s[14:15] op_sel_hi:[1,0,0]
	v_pk_mul_f32 v[6:7], v[14:15], v[6:7]
	v_rcp_f32_e32 v24, v24
	v_rcp_f32_e32 v25, v25
	v_pk_fma_f32 v[18:19], v[18:19], s[14:15], s[14:15] op_sel_hi:[1,0,0]
	v_pk_fma_f32 v[22:23], v[22:23], s[14:15], s[14:15] op_sel_hi:[1,0,0]
	v_pk_mul_f32 v[6:7], v[6:7], v[20:21]
	v_pk_mul_f32 v[2:3], v[10:11], v[2:3]
	v_rcp_f32_e32 v18, v18
	v_rcp_f32_e32 v19, v19
	v_rcp_f32_e32 v22, v22
	v_rcp_f32_e32 v23, v23
	v_pk_mul_f32 v[2:3], v[2:3], v[24:25]
	v_med3_f32 v10, v6, s56, v157
	v_med3_f32 v7, v7, s56, v157
	s_nop 0
	v_cvt_pk_fp8_f32 v6, v10, v7
	v_med3_f32 v2, v2, s56, v157
	v_med3_f32 v3, v3, s56, v157
	s_nop 0
	v_cvt_pk_fp8_f32 v7, v2, v3
	v_pk_mul_f32 v[8:9], v[16:17], v[8:9]
	v_pk_mul_f32 v[4:5], v[12:13], v[4:5]
	v_pk_mul_f32 v[8:9], v[8:9], v[18:19]
	v_pk_mul_f32 v[4:5], v[4:5], v[22:23]
	v_med3_f32 v8, v8, s56, v157
	v_med3_f32 v9, v9, s56, v157
	v_med3_f32 v2, v4, s56, v157
	v_med3_f32 v3, v5, s56, v157
	v_cvt_pk_fp8_f32 v6, v8, v9 op_sel:[0,0,1]
	v_cvt_pk_fp8_f32 v7, v2, v3 op_sel:[0,0,1]
	v_add_u32_e32 v26, 0xb0, v158
	v_mad_i64_i32 v[2:3], s[26:27], v26, s55, v[150:151]
	v_lshl_add_u64 v[2:3], v[2:3], 0, v[148:149]
	s_andn2_b64 vcc, exec, s[2:3]
	s_mov_b64 s[2:3], -1
	global_store_dwordx2 v[2:3], v[6:7], off
	s_cbranch_vccnz .LBB0_1078
	s_andn2_b64 vcc, exec, s[4:5]
	s_cbranch_vccnz .LBB0_1077
	s_barrier
	s_branch .LBB0_1077
